# LDS-read hoist register pool widened to v<240 in the attention MFMA segments
# baseline (speedup 1.0000x reference)
.LBB0_528:
	ds_read_b128 v[88:91], v129
	ds_read_b128 v[92:95], v129 offset:1024
	ds_read_b128 v[96:99], v130
	ds_read_b128 v[152:155], v130 offset:1024
	ds_read_b128 v[176:179], v131
	ds_read_b128 v[180:183], v131 offset:1024
	ds_read_b128 v[184:187], v132
	ds_read_b128 v[188:191], v132 offset:1024
	ds_read_b128 v[192:195], v129 offset:8192
	ds_read_b128 v[196:199], v129 offset:9216
	ds_read_b128 v[200:203], v130 offset:8192
	ds_read_b128 v[204:207], v130 offset:9216
	ds_read_b128 v[208:211], v131 offset:8192
	ds_read_b128 v[212:215], v131 offset:9216
	ds_read_b128 v[216:219], v132 offset:8192
	s_and_b64 vcc, exec, s[10:11]
	s_waitcnt lgkmcnt(11)
	v_mfma_f32_16x16x32_bf16 v[72:75], v[88:91], v[0:3], v[240:243]
	ds_read_b128 v[220:223], v132 offset:9216
	ds_read_b64_tr_b16 v[224:225], v142 offset:49152
	ds_read_b64_tr_b16 v[226:227], v146 offset:49152
	ds_read_b64_tr_b16 v[230:231], v146 offset:57344
	v_mfma_f32_16x16x32_bf16 v[72:75], v[96:99], v[4:7], v[72:75]
	v_mfma_f32_16x16x32_bf16 v[76:79], v[92:95], v[0:3], v[240:243]
	s_waitcnt lgkmcnt(11)
	v_mfma_f32_16x16x32_bf16 v[72:75], v[176:179], v[8:11], v[72:75]
	ds_read_b64_tr_b16 v[228:229], v142 offset:57344
	ds_read_b64_tr_b16 v[232:233], v136 offset:49152
	ds_read_b64_tr_b16 v[234:235], v137 offset:49152
	ds_read_b64_tr_b16 v[238:239], v137 offset:57344
	v_mfma_f32_16x16x32_bf16 v[84:87], v[184:187], v[12:15], v[72:75]
	v_mfma_f32_16x16x32_bf16 v[72:75], v[152:155], v[4:7], v[76:79]
	v_mfma_f32_16x16x32_bf16 v[72:75], v[180:183], v[8:11], v[72:75]
	v_mfma_f32_16x16x32_bf16 v[80:83], v[188:191], v[12:15], v[72:75]
	s_waitcnt lgkmcnt(11)
	s_nop 5
	v_mfma_f32_16x16x32_bf16 v[72:75], v[192:195], v[0:3], v[240:243]
	ds_read_b64_tr_b16 v[236:237], v136 offset:57344
	ds_read_b64_tr_b16 v[88:89], v139 offset:49152
	ds_read_b64_tr_b16 v[90:91], v145 offset:49152
	ds_read_b64_tr_b16 v[98:99], v145 offset:57344
	v_mfma_f32_16x16x32_bf16 v[72:75], v[200:203], v[4:7], v[72:75]
	s_waitcnt lgkmcnt(11)
	v_mfma_f32_16x16x32_bf16 v[72:75], v[208:211], v[8:11], v[72:75]
	ds_read_b64_tr_b16 v[96:97], v139 offset:57344
	ds_read_b64_tr_b16 v[92:93], v140 offset:49152
	ds_read_b64_tr_b16 v[94:95], v147 offset:49152
	ds_read_b64_tr_b16 v[178:179], v147 offset:57344
	v_mfma_f32_16x16x32_bf16 v[76:79], v[216:219], v[12:15], v[72:75]
	v_mfma_f32_16x16x32_bf16 v[72:75], v[196:199], v[0:3], v[240:243]
	v_mfma_f32_16x16x32_bf16 v[72:75], v[204:207], v[4:7], v[72:75]
	s_waitcnt lgkmcnt(10)
	v_mfma_f32_16x16x32_bf16 v[60:63], v[224:227], v[68:71], v[60:63]
	ds_read_b64_tr_b16 v[176:177], v140 offset:57344
	ds_read_b64_tr_b16 v[184:185], v148 offset:49152
	ds_read_b64_tr_b16 v[186:187], v149 offset:49152
	ds_read_b64_tr_b16 v[154:155], v149 offset:57344
	ds_read_b64_tr_b16 v[152:153], v148 offset:57344
	v_mfma_f32_16x16x32_bf16 v[60:63], v[228:231], v[64:67], v[60:63]
	s_waitcnt lgkmcnt(11)
	v_mfma_f32_16x16x32_bf16 v[52:55], v[232:235], v[68:71], v[52:55]
	ds_read_b64_tr_b16 v[180:181], v133 offset:49152
	ds_read_b64_tr_b16 v[182:183], v134 offset:49152
	ds_read_b64_tr_b16 v[190:191], v134 offset:57344
	ds_read_b64_tr_b16 v[188:189], v133 offset:57344
	v_mfma_f32_16x16x32_bf16 v[52:55], v[236:239], v[64:67], v[52:55]
	s_waitcnt lgkmcnt(11)
	v_mfma_f32_16x16x32_bf16 v[48:51], v[88:91], v[68:71], v[48:51]
	ds_read_b64_tr_b16 v[192:193], v135 offset:49152
	ds_read_b64_tr_b16 v[194:195], v138 offset:49152
	ds_read_b64_tr_b16 v[202:203], v138 offset:57344
	ds_read_b64_tr_b16 v[200:201], v135 offset:57344
	v_mfma_f32_16x16x32_bf16 v[48:51], v[96:99], v[64:67], v[48:51]
	s_waitcnt lgkmcnt(11)
	v_mfma_f32_16x16x32_bf16 v[56:59], v[92:95], v[68:71], v[56:59]
	ds_read_b64_tr_b16 v[208:209], v141 offset:49152
	ds_read_b64_tr_b16 v[210:211], v143 offset:49152
	ds_read_b64_tr_b16 v[218:219], v143 offset:57344
	ds_read_b64_tr_b16 v[216:217], v141 offset:57344
	v_mfma_f32_16x16x32_bf16 v[56:59], v[176:179], v[64:67], v[56:59]
	s_waitcnt lgkmcnt(11)
	v_mfma_f32_16x16x32_bf16 v[32:35], v[184:187], v[68:71], v[32:35]
	v_mfma_f32_16x16x32_bf16 v[32:35], v[152:155], v[64:67], v[32:35]
	s_waitcnt lgkmcnt(7)
	v_mfma_f32_16x16x32_bf16 v[36:39], v[180:183], v[68:71], v[36:39]
	v_mfma_f32_16x16x32_bf16 v[36:39], v[188:191], v[64:67], v[36:39]
	s_waitcnt lgkmcnt(3)
	v_mfma_f32_16x16x32_bf16 v[40:43], v[192:195], v[68:71], v[40:43]
	v_mfma_f32_16x16x32_bf16 v[40:43], v[200:203], v[64:67], v[40:43]
	v_mfma_f32_16x16x32_bf16 v[72:75], v[212:215], v[8:11], v[72:75]
	s_waitcnt lgkmcnt(0)
	v_mfma_f32_16x16x32_bf16 v[44:47], v[208:211], v[68:71], v[44:47]
	v_mfma_f32_16x16x32_bf16 v[72:75], v[220:223], v[12:15], v[72:75]
	v_mfma_f32_16x16x32_bf16 v[44:47], v[216:219], v[64:67], v[44:47]
	s_cbranch_vccnz .LBB0_530
	v_add_u32_e32 v64, 0, v109
	s_waitcnt vmcnt(3)
	ds_write_b128 v100, v[16:19] offset:16384
	s_waitcnt vmcnt(2)
	ds_write_b128 v124, v[20:23] offset:16384
	s_waitcnt vmcnt(1)
	ds_write_b128 v64, v[24:27] offset:32768
	v_add_u32_e32 v64, 0, v112
	s_waitcnt vmcnt(0)
	ds_write_b128 v64, v[28:31] offset:32768

.LBB0_536:
	ds_read_b128 v[168:171], v129 offset:16384
	ds_read_b128 v[172:175], v130 offset:16384
	ds_read_b128 v[176:179], v131 offset:16384
	ds_read_b128 v[180:183], v129 offset:17408
	ds_read_b128 v[184:187], v132 offset:16384
	ds_read_b128 v[188:191], v130 offset:17408
	ds_read_b128 v[192:195], v131 offset:17408
	ds_read_b128 v[196:199], v129 offset:24576
	ds_read_b128 v[200:203], v132 offset:17408
	ds_read_b128 v[204:207], v130 offset:24576
	ds_read_b128 v[208:211], v131 offset:24576
	ds_read_b128 v[212:215], v129 offset:25600
	ds_read_b128 v[216:219], v132 offset:24576
	ds_read_b128 v[220:223], v130 offset:25600
	ds_read_b128 v[224:227], v131 offset:25600
	v_sub_f32_e32 v64, v84, v96
	v_exp_f32_e32 v96, v64
	v_sub_f32_e32 v64, v85, v97
	v_exp_f32_e32 v97, v64
	v_sub_f32_e32 v64, v86, v98
	v_exp_f32_e32 v98, v64
	v_sub_f32_e32 v64, v87, v99
	v_exp_f32_e32 v99, v64
	v_sub_f32_e32 v64, v80, v92
	v_exp_f32_e32 v153, v64
	v_sub_f32_e32 v64, v81, v93
	v_exp_f32_e32 v154, v64
	v_sub_f32_e32 v64, v82, v94
	v_exp_f32_e32 v155, v64
	v_sub_f32_e32 v64, v83, v95
	s_waitcnt lgkmcnt(11)
	v_mfma_f32_16x16x32_bf16 v[84:87], v[168:171], v[0:3], v[240:243]
	ds_read_b128 v[228:231], v132 offset:25600
	ds_read_b64_tr_b16 v[232:233], v142 offset:32768
	ds_read_b64_tr_b16 v[234:235], v146 offset:32768
	ds_read_b64_tr_b16 v[238:239], v146 offset:40960
	v_exp_f32_e32 v156, v64
	v_sub_f32_e32 v64, v76, v88
	v_exp_f32_e32 v157, v64
	v_mfma_f32_16x16x32_bf16 v[92:95], v[180:183], v[0:3], v[240:243]
	v_sub_f32_e32 v64, v77, v89
	v_sub_f32_e32 v70, v73, v67
	v_mfma_f32_16x16x32_bf16 v[84:87], v[172:175], v[4:7], v[84:87]
	v_exp_f32_e32 v158, v64
	v_sub_f32_e32 v64, v78, v90
	v_exp_f32_e32 v159, v64
	v_sub_f32_e32 v64, v79, v91
	s_waitcnt lgkmcnt(10)
	v_mfma_f32_16x16x32_bf16 v[88:91], v[188:191], v[4:7], v[92:95]
	ds_read_b64_tr_b16 v[236:237], v142 offset:40960
	ds_read_b64_tr_b16 v[168:169], v136 offset:32768
	ds_read_b64_tr_b16 v[170:171], v137 offset:32768
	ds_read_b64_tr_b16 v[182:183], v137 offset:40960
	ds_read_b64_tr_b16 v[180:181], v136 offset:40960
	v_exp_f32_e32 v160, v64
	v_mfma_f32_16x16x32_bf16 v[80:83], v[176:179], v[8:11], v[84:87]
	v_sub_f32_e32 v64, v72, v66
	v_exp_f32_e32 v161, v64
	v_mfma_f32_16x16x32_bf16 v[76:79], v[192:195], v[8:11], v[88:91]
	v_sub_f32_e32 v68, v74, v68
	s_and_b64 vcc, exec, s[10:11]
	v_mfma_f32_16x16x32_bf16 v[92:95], v[196:199], v[0:3], v[240:243]
	v_mfma_f32_16x16x32_bf16 v[80:83], v[184:187], v[12:15], v[80:83]
	v_exp_f32_e32 v162, v70
	v_exp_f32_e32 v163, v68
	v_mfma_f32_16x16x32_bf16 v[76:79], v[200:203], v[12:15], v[76:79]
	s_waitcnt lgkmcnt(11)
	v_mfma_f32_16x16x32_bf16 v[88:91], v[204:207], v[4:7], v[92:95]
	ds_read_b64_tr_b16 v[172:173], v139 offset:32768
	ds_read_b64_tr_b16 v[174:175], v145 offset:32768
	ds_read_b64_tr_b16 v[190:191], v145 offset:40960
	ds_read_b64_tr_b16 v[188:189], v139 offset:40960
	v_sub_f32_e32 v68, v75, v69
	v_mfma_f32_16x16x32_bf16 v[84:87], v[208:211], v[8:11], v[88:91]
	v_cvt_pk_bf16_f32 v92, v96, v97
	v_cvt_pk_bf16_f32 v93, v98, v99
	v_cvt_pk_bf16_f32 v94, v153, v154
	v_mfma_f32_16x16x32_bf16 v[64:67], v[216:219], v[12:15], v[84:87]
	v_cvt_pk_bf16_f32 v95, v155, v156
	v_mfma_f32_16x16x32_bf16 v[84:87], v[212:215], v[0:3], v[240:243]
	v_exp_f32_e32 v164, v68
	s_waitcnt lgkmcnt(11)
	v_mfma_f32_16x16x32_bf16 v[84:87], v[220:223], v[4:7], v[84:87]
	ds_read_b64_tr_b16 v[176:177], v140 offset:32768
	ds_read_b64_tr_b16 v[178:179], v147 offset:32768
	ds_read_b64_tr_b16 v[194:195], v147 offset:40960
	ds_read_b64_tr_b16 v[192:193], v140 offset:40960
	v_mfma_f32_16x16x32_bf16 v[68:71], v[224:227], v[8:11], v[84:87]
	s_nop 2
	v_cvt_pk_bf16_f32 v84, v157, v158
	v_mfma_f32_16x16x32_bf16 v[68:71], v[228:231], v[12:15], v[68:71]
	v_cvt_pk_bf16_f32 v85, v159, v160
	v_cvt_pk_bf16_f32 v86, v161, v162
	s_waitcnt lgkmcnt(11)
	v_mfma_f32_16x16x32_bf16 v[60:63], v[232:235], v[92:95], v[60:63]
	ds_read_b64_tr_b16 v[196:197], v148 offset:32768
	ds_read_b64_tr_b16 v[198:199], v149 offset:32768
	ds_read_b64_tr_b16 v[186:187], v149 offset:40960
	ds_read_b64_tr_b16 v[184:185], v148 offset:40960
	v_cvt_pk_bf16_f32 v87, v163, v164
	s_nop 1
	v_mfma_f32_16x16x32_bf16 v[60:63], v[236:239], v[84:87], v[60:63]
	s_waitcnt lgkmcnt(11)
	v_mfma_f32_16x16x32_bf16 v[52:55], v[168:171], v[92:95], v[52:55]
	ds_read_b64_tr_b16 v[200:201], v133 offset:32768
	ds_read_b64_tr_b16 v[202:203], v134 offset:32768
	ds_read_b64_tr_b16 v[206:207], v134 offset:40960
	ds_read_b64_tr_b16 v[204:205], v133 offset:40960
	v_mfma_f32_16x16x32_bf16 v[52:55], v[180:183], v[84:87], v[52:55]
	s_waitcnt lgkmcnt(11)
	v_mfma_f32_16x16x32_bf16 v[48:51], v[172:175], v[92:95], v[48:51]
	ds_read_b64_tr_b16 v[208:209], v135 offset:32768
	ds_read_b64_tr_b16 v[210:211], v138 offset:32768
	ds_read_b64_tr_b16 v[218:219], v138 offset:40960
	ds_read_b64_tr_b16 v[216:217], v135 offset:40960
	v_mfma_f32_16x16x32_bf16 v[48:51], v[188:191], v[84:87], v[48:51]
	s_waitcnt lgkmcnt(11)
	v_mfma_f32_16x16x32_bf16 v[56:59], v[176:179], v[92:95], v[56:59]
	ds_read_b64_tr_b16 v[212:213], v141 offset:32768
	ds_read_b64_tr_b16 v[214:215], v143 offset:32768
	ds_read_b64_tr_b16 v[222:223], v143 offset:40960
	ds_read_b64_tr_b16 v[220:221], v141 offset:40960
	v_mfma_f32_16x16x32_bf16 v[56:59], v[192:195], v[84:87], v[56:59]
	s_waitcnt lgkmcnt(11)
	v_mfma_f32_16x16x32_bf16 v[32:35], v[196:199], v[92:95], v[32:35]
	v_mfma_f32_16x16x32_bf16 v[32:35], v[184:187], v[84:87], v[32:35]
	s_waitcnt lgkmcnt(7)
	v_mfma_f32_16x16x32_bf16 v[36:39], v[200:203], v[92:95], v[36:39]
	v_mfma_f32_16x16x32_bf16 v[36:39], v[204:207], v[84:87], v[36:39]
	s_waitcnt lgkmcnt(3)
	v_mfma_f32_16x16x32_bf16 v[40:43], v[208:211], v[92:95], v[40:43]
	v_mfma_f32_16x16x32_bf16 v[40:43], v[216:219], v[84:87], v[40:43]
	s_waitcnt lgkmcnt(0)
	v_mfma_f32_16x16x32_bf16 v[44:47], v[212:215], v[92:95], v[44:47]
	v_mfma_f32_16x16x32_bf16 v[44:47], v[220:223], v[84:87], v[44:47]
	s_cbranch_vccnz .LBB0_538
	v_add_u32_e32 v72, 0, v109
	s_waitcnt vmcnt(3)
	ds_write_b128 v100, v[16:19]
	s_waitcnt vmcnt(2)
	ds_write_b128 v124, v[20:23]
	s_waitcnt vmcnt(1)
	ds_write_b128 v72, v[24:27] offset:49152
	v_add_u32_e32 v72, 0, v112
	s_waitcnt vmcnt(0)
	ds_write_b128 v72, v[28:31] offset:49152

.LBB0_567:
	ds_read_b128 v[88:91], v129
	ds_read_b128 v[92:95], v129 offset:1024
	ds_read_b128 v[96:99], v130
	ds_read_b128 v[152:155], v130 offset:1024
	ds_read_b128 v[172:175], v131
	ds_read_b128 v[176:179], v131 offset:1024
	ds_read_b128 v[180:183], v132
	ds_read_b128 v[184:187], v132 offset:1024
	ds_read_b128 v[188:191], v129 offset:8192
	ds_read_b128 v[192:195], v129 offset:9216
	ds_read_b128 v[196:199], v130 offset:8192
	ds_read_b128 v[200:203], v130 offset:9216
	ds_read_b128 v[204:207], v131 offset:8192
	ds_read_b128 v[208:211], v131 offset:9216
	ds_read_b128 v[212:215], v132 offset:8192
	s_and_b64 vcc, exec, s[10:11]
	s_waitcnt lgkmcnt(11)
	v_mfma_f32_16x16x32_bf16 v[72:75], v[88:91], v[0:3], v[240:243]
	ds_read_b128 v[216:219], v132 offset:9216
	ds_read_b64_tr_b16 v[220:221], v146 offset:49152
	ds_read_b64_tr_b16 v[222:223], v148 offset:49152
	ds_read_b64_tr_b16 v[226:227], v148 offset:57344
	v_mfma_f32_16x16x32_bf16 v[72:75], v[96:99], v[4:7], v[72:75]
	v_mfma_f32_16x16x32_bf16 v[76:79], v[92:95], v[0:3], v[240:243]
	s_waitcnt lgkmcnt(11)
	v_mfma_f32_16x16x32_bf16 v[72:75], v[172:175], v[8:11], v[72:75]
	ds_read_b64_tr_b16 v[224:225], v146 offset:57344
	ds_read_b64_tr_b16 v[228:229], v139 offset:49152
	ds_read_b64_tr_b16 v[230:231], v142 offset:49152
	ds_read_b64_tr_b16 v[234:235], v142 offset:57344
	v_mfma_f32_16x16x32_bf16 v[84:87], v[180:183], v[12:15], v[72:75]
	v_mfma_f32_16x16x32_bf16 v[72:75], v[152:155], v[4:7], v[76:79]
	v_mfma_f32_16x16x32_bf16 v[72:75], v[176:179], v[8:11], v[72:75]
	v_mfma_f32_16x16x32_bf16 v[80:83], v[184:187], v[12:15], v[72:75]
	s_waitcnt lgkmcnt(11)
	s_nop 5
	v_mfma_f32_16x16x32_bf16 v[72:75], v[188:191], v[0:3], v[240:243]
	ds_read_b64_tr_b16 v[232:233], v139 offset:57344
	ds_read_b64_tr_b16 v[236:237], v141 offset:49152
	ds_read_b64_tr_b16 v[238:239], v145 offset:49152
	ds_read_b64_tr_b16 v[90:91], v145 offset:57344
	v_mfma_f32_16x16x32_bf16 v[72:75], v[196:199], v[4:7], v[72:75]
	s_waitcnt lgkmcnt(11)
	v_mfma_f32_16x16x32_bf16 v[72:75], v[204:207], v[8:11], v[72:75]
	ds_read_b64_tr_b16 v[88:89], v141 offset:57344
	ds_read_b64_tr_b16 v[96:97], v140 offset:49152
	ds_read_b64_tr_b16 v[98:99], v143 offset:49152
	ds_read_b64_tr_b16 v[94:95], v143 offset:57344
	v_mfma_f32_16x16x32_bf16 v[76:79], v[212:215], v[12:15], v[72:75]
	v_mfma_f32_16x16x32_bf16 v[72:75], v[192:195], v[0:3], v[240:243]
	v_mfma_f32_16x16x32_bf16 v[72:75], v[200:203], v[4:7], v[72:75]
	s_waitcnt lgkmcnt(10)
	v_mfma_f32_16x16x32_bf16 v[60:63], v[220:223], v[68:71], v[60:63]
	ds_read_b64_tr_b16 v[92:93], v140 offset:57344
	ds_read_b64_tr_b16 v[172:173], v147 offset:49152
	ds_read_b64_tr_b16 v[174:175], v149 offset:49152
	ds_read_b64_tr_b16 v[182:183], v149 offset:57344
	ds_read_b64_tr_b16 v[180:181], v147 offset:57344
	v_mfma_f32_16x16x32_bf16 v[60:63], v[224:227], v[64:67], v[60:63]
	s_waitcnt lgkmcnt(11)
	v_mfma_f32_16x16x32_bf16 v[56:59], v[228:231], v[68:71], v[56:59]
	ds_read_b64_tr_b16 v[152:153], v133 offset:49152
	ds_read_b64_tr_b16 v[154:155], v134 offset:49152
	ds_read_b64_tr_b16 v[178:179], v134 offset:57344
	ds_read_b64_tr_b16 v[176:177], v133 offset:57344
	v_mfma_f32_16x16x32_bf16 v[56:59], v[232:235], v[64:67], v[56:59]
	s_waitcnt lgkmcnt(11)
	v_mfma_f32_16x16x32_bf16 v[52:55], v[236:239], v[68:71], v[52:55]
	ds_read_b64_tr_b16 v[184:185], v135 offset:49152
	ds_read_b64_tr_b16 v[186:187], v136 offset:49152
	ds_read_b64_tr_b16 v[190:191], v136 offset:57344
	ds_read_b64_tr_b16 v[188:189], v135 offset:57344
	v_mfma_f32_16x16x32_bf16 v[52:55], v[88:91], v[64:67], v[52:55]
	s_waitcnt lgkmcnt(11)
	v_mfma_f32_16x16x32_bf16 v[48:51], v[96:99], v[68:71], v[48:51]
	ds_read_b64_tr_b16 v[196:197], v137 offset:49152
	ds_read_b64_tr_b16 v[198:199], v138 offset:49152
	ds_read_b64_tr_b16 v[206:207], v138 offset:57344
	ds_read_b64_tr_b16 v[204:205], v137 offset:57344
	v_mfma_f32_16x16x32_bf16 v[48:51], v[92:95], v[64:67], v[48:51]
	s_waitcnt lgkmcnt(11)
	v_mfma_f32_16x16x32_bf16 v[32:35], v[172:175], v[68:71], v[32:35]
	v_mfma_f32_16x16x32_bf16 v[32:35], v[180:183], v[64:67], v[32:35]
	s_waitcnt lgkmcnt(7)
	v_mfma_f32_16x16x32_bf16 v[36:39], v[152:155], v[68:71], v[36:39]
	v_mfma_f32_16x16x32_bf16 v[36:39], v[176:179], v[64:67], v[36:39]
	s_waitcnt lgkmcnt(3)
	v_mfma_f32_16x16x32_bf16 v[40:43], v[184:187], v[68:71], v[40:43]
	v_mfma_f32_16x16x32_bf16 v[40:43], v[188:191], v[64:67], v[40:43]
	v_mfma_f32_16x16x32_bf16 v[72:75], v[208:211], v[8:11], v[72:75]
	s_waitcnt lgkmcnt(0)
	v_mfma_f32_16x16x32_bf16 v[44:47], v[196:199], v[68:71], v[44:47]
	v_mfma_f32_16x16x32_bf16 v[72:75], v[216:219], v[12:15], v[72:75]
	v_mfma_f32_16x16x32_bf16 v[44:47], v[204:207], v[64:67], v[44:47]
	s_cbranch_vccnz .LBB0_569
	v_add_u32_e32 v64, 0, v109
	s_waitcnt vmcnt(3)
	ds_write_b128 v100, v[16:19] offset:16384
	s_waitcnt vmcnt(2)
	ds_write_b128 v124, v[20:23] offset:16384
	s_waitcnt vmcnt(1)
	ds_write_b128 v64, v[24:27] offset:32768
	v_add_u32_e32 v64, 0, v112
	s_waitcnt vmcnt(0)
	ds_write_b128 v64, v[28:31] offset:32768

.LBB0_575:
	ds_read_b128 v[164:167], v129 offset:16384
	ds_read_b128 v[168:171], v130 offset:16384
	ds_read_b128 v[172:175], v131 offset:16384
	ds_read_b128 v[176:179], v129 offset:17408
	ds_read_b128 v[180:183], v132 offset:16384
	ds_read_b128 v[184:187], v130 offset:17408
	ds_read_b128 v[188:191], v131 offset:17408
	ds_read_b128 v[192:195], v129 offset:24576
	ds_read_b128 v[196:199], v132 offset:17408
	ds_read_b128 v[200:203], v130 offset:24576
	ds_read_b128 v[204:207], v131 offset:24576
	ds_read_b128 v[208:211], v129 offset:25600
	ds_read_b128 v[212:215], v132 offset:24576
	ds_read_b128 v[216:219], v130 offset:25600
	ds_read_b128 v[220:223], v131 offset:25600
	v_sub_f32_e32 v64, v84, v96
	v_exp_f32_e32 v96, v64
	v_sub_f32_e32 v64, v85, v97
	v_exp_f32_e32 v97, v64
	v_sub_f32_e32 v64, v86, v98
	v_exp_f32_e32 v98, v64
	v_sub_f32_e32 v64, v87, v99
	v_exp_f32_e32 v99, v64
	v_sub_f32_e32 v64, v80, v92
	v_exp_f32_e32 v152, v64
	v_sub_f32_e32 v64, v81, v93
	v_exp_f32_e32 v153, v64
	v_sub_f32_e32 v64, v82, v94
	v_exp_f32_e32 v154, v64
	v_sub_f32_e32 v64, v83, v95
	s_waitcnt lgkmcnt(11)
	v_mfma_f32_16x16x32_bf16 v[84:87], v[164:167], v[0:3], v[240:243]
	ds_read_b128 v[224:227], v132 offset:25600
	ds_read_b64_tr_b16 v[228:229], v146 offset:32768
	ds_read_b64_tr_b16 v[230:231], v148 offset:32768
	ds_read_b64_tr_b16 v[234:235], v148 offset:40960
	v_exp_f32_e32 v155, v64
	v_sub_f32_e32 v64, v76, v88
	v_mfma_f32_16x16x32_bf16 v[84:87], v[168:171], v[4:7], v[84:87]
	v_exp_f32_e32 v156, v64
	v_sub_f32_e32 v64, v77, v89
	v_mfma_f32_16x16x32_bf16 v[92:95], v[176:179], v[0:3], v[240:243]
	v_exp_f32_e32 v157, v64
	v_sub_f32_e32 v64, v78, v90
	v_exp_f32_e32 v158, v64
	v_sub_f32_e32 v64, v79, v91
	s_waitcnt lgkmcnt(10)
	v_mfma_f32_16x16x32_bf16 v[88:91], v[184:187], v[4:7], v[92:95]
	ds_read_b64_tr_b16 v[232:233], v146 offset:40960
	ds_read_b64_tr_b16 v[236:237], v139 offset:32768
	ds_read_b64_tr_b16 v[238:239], v142 offset:32768
	ds_read_b64_tr_b16 v[166:167], v142 offset:40960
	ds_read_b64_tr_b16 v[164:165], v139 offset:40960
	v_exp_f32_e32 v159, v64
	v_mfma_f32_16x16x32_bf16 v[80:83], v[172:175], v[8:11], v[84:87]
	v_sub_f32_e32 v64, v72, v66
	v_sub_f32_e32 v70, v73, v67
	v_mfma_f32_16x16x32_bf16 v[76:79], v[188:191], v[8:11], v[88:91]
	v_sub_f32_e32 v68, v74, v68
	s_and_b64 vcc, exec, s[10:11]
	v_mfma_f32_16x16x32_bf16 v[92:95], v[192:195], v[0:3], v[240:243]
	v_mfma_f32_16x16x32_bf16 v[76:79], v[196:199], v[12:15], v[76:79]
	s_waitcnt lgkmcnt(11)
	v_mfma_f32_16x16x32_bf16 v[88:91], v[200:203], v[4:7], v[92:95]
	ds_read_b64_tr_b16 v[168:169], v141 offset:32768
	ds_read_b64_tr_b16 v[170:171], v145 offset:32768
	ds_read_b64_tr_b16 v[178:179], v145 offset:40960
	ds_read_b64_tr_b16 v[176:177], v141 offset:40960
	v_mfma_f32_16x16x32_bf16 v[80:83], v[180:183], v[12:15], v[80:83]
	v_exp_f32_e32 v160, v64
	v_exp_f32_e32 v161, v70
	v_mfma_f32_16x16x32_bf16 v[84:87], v[204:207], v[8:11], v[88:91]
	v_exp_f32_e32 v162, v68
	v_mfma_f32_16x16x32_bf16 v[64:67], v[212:215], v[12:15], v[84:87]
	v_sub_f32_e32 v68, v75, v69
	v_exp_f32_e32 v163, v68
	v_mfma_f32_16x16x32_bf16 v[84:87], v[208:211], v[0:3], v[240:243]
	v_cvt_pk_bf16_f32 v92, v96, v97
	v_cvt_pk_bf16_f32 v93, v98, v99
	s_waitcnt lgkmcnt(11)
	v_mfma_f32_16x16x32_bf16 v[84:87], v[216:219], v[4:7], v[84:87]
	ds_read_b64_tr_b16 v[184:185], v140 offset:32768
	ds_read_b64_tr_b16 v[186:187], v143 offset:32768
	ds_read_b64_tr_b16 v[174:175], v143 offset:40960
	ds_read_b64_tr_b16 v[172:173], v140 offset:40960
	v_cvt_pk_bf16_f32 v94, v152, v153
	v_cvt_pk_bf16_f32 v95, v154, v155
	v_mfma_f32_16x16x32_bf16 v[68:71], v[220:223], v[8:11], v[84:87]
	s_nop 2
	v_cvt_pk_bf16_f32 v84, v156, v157
	v_mfma_f32_16x16x32_bf16 v[68:71], v[224:227], v[12:15], v[68:71]
	v_cvt_pk_bf16_f32 v85, v158, v159
	v_cvt_pk_bf16_f32 v86, v160, v161
	s_waitcnt lgkmcnt(11)
	v_mfma_f32_16x16x32_bf16 v[60:63], v[228:231], v[92:95], v[60:63]
	ds_read_b64_tr_b16 v[188:189], v147 offset:32768
	ds_read_b64_tr_b16 v[190:191], v149 offset:32768
	ds_read_b64_tr_b16 v[194:195], v149 offset:40960
	ds_read_b64_tr_b16 v[192:193], v147 offset:40960
	v_cvt_pk_bf16_f32 v87, v162, v163
	s_nop 1
	v_mfma_f32_16x16x32_bf16 v[60:63], v[232:235], v[84:87], v[60:63]
	s_waitcnt lgkmcnt(11)
	v_mfma_f32_16x16x32_bf16 v[56:59], v[236:239], v[92:95], v[56:59]
	ds_read_b64_tr_b16 v[196:197], v133 offset:32768
	ds_read_b64_tr_b16 v[198:199], v134 offset:32768
	ds_read_b64_tr_b16 v[202:203], v134 offset:40960
	ds_read_b64_tr_b16 v[200:201], v133 offset:40960
	v_mfma_f32_16x16x32_bf16 v[56:59], v[164:167], v[84:87], v[56:59]
	s_waitcnt lgkmcnt(11)
	v_mfma_f32_16x16x32_bf16 v[52:55], v[168:171], v[92:95], v[52:55]
	ds_read_b64_tr_b16 v[180:181], v135 offset:32768
	ds_read_b64_tr_b16 v[182:183], v136 offset:32768
	ds_read_b64_tr_b16 v[206:207], v136 offset:40960
	ds_read_b64_tr_b16 v[204:205], v135 offset:40960
	v_mfma_f32_16x16x32_bf16 v[52:55], v[176:179], v[84:87], v[52:55]
	s_waitcnt lgkmcnt(11)
	v_mfma_f32_16x16x32_bf16 v[48:51], v[184:187], v[92:95], v[48:51]
	ds_read_b64_tr_b16 v[212:213], v137 offset:32768
	ds_read_b64_tr_b16 v[214:215], v138 offset:32768
	ds_read_b64_tr_b16 v[210:211], v138 offset:40960
	ds_read_b64_tr_b16 v[208:209], v137 offset:40960
	v_mfma_f32_16x16x32_bf16 v[48:51], v[172:175], v[84:87], v[48:51]
	s_waitcnt lgkmcnt(11)
	v_mfma_f32_16x16x32_bf16 v[32:35], v[188:191], v[92:95], v[32:35]
	v_mfma_f32_16x16x32_bf16 v[32:35], v[192:195], v[84:87], v[32:35]
	s_waitcnt lgkmcnt(7)
	v_mfma_f32_16x16x32_bf16 v[36:39], v[196:199], v[92:95], v[36:39]
	v_mfma_f32_16x16x32_bf16 v[36:39], v[200:203], v[84:87], v[36:39]
	s_waitcnt lgkmcnt(3)
	v_mfma_f32_16x16x32_bf16 v[40:43], v[180:183], v[92:95], v[40:43]
	v_mfma_f32_16x16x32_bf16 v[40:43], v[204:207], v[84:87], v[40:43]
	s_waitcnt lgkmcnt(0)
	v_mfma_f32_16x16x32_bf16 v[44:47], v[212:215], v[92:95], v[44:47]
	v_mfma_f32_16x16x32_bf16 v[44:47], v[208:211], v[84:87], v[44:47]
	s_cbranch_vccnz .LBB0_577
	v_add_u32_e32 v72, 0, v109
	s_waitcnt vmcnt(3)
	ds_write_b128 v100, v[16:19]
	s_waitcnt vmcnt(2)
	ds_write_b128 v124, v[20:23]
	s_waitcnt vmcnt(1)
	ds_write_b128 v72, v[24:27] offset:49152
	v_add_u32_e32 v72, 0, v112
	s_waitcnt vmcnt(0)
	ds_write_b128 v72, v[28:31] offset:49152

.LBB0_639:
	ds_read_b128 v[88:91], v128
	ds_read_b128 v[92:95], v128 offset:1024
	ds_read_b128 v[156:159], v129
	ds_read_b128 v[188:191], v129 offset:1024
	ds_read_b128 v[192:195], v130
	ds_read_b128 v[196:199], v130 offset:1024
	ds_read_b128 v[200:203], v131
	ds_read_b128 v[204:207], v131 offset:1024
	ds_read_b128 v[208:211], v128 offset:8192
	ds_read_b128 v[212:215], v128 offset:9216
	ds_read_b128 v[216:219], v129 offset:8192
	ds_read_b128 v[220:223], v129 offset:9216
	ds_read_b128 v[224:227], v130 offset:8192
	ds_read_b128 v[228:231], v130 offset:9216
	ds_read_b128 v[232:235], v131 offset:8192
	s_and_b64 vcc, exec, s[10:11]
	s_waitcnt lgkmcnt(11)
	v_mfma_f32_16x16x32_bf16 v[72:75], v[88:91], v[0:3], 0
	ds_read_b128 v[236:239], v131 offset:9216
	ds_read_b64_tr_b16 v[88:89], v140 offset:49152
	ds_read_b64_tr_b16 v[90:91], v141 offset:49152
	v_mfma_f32_16x16x32_bf16 v[80:83], v[92:95], v[0:3], 0
	ds_read_b64_tr_b16 v[94:95], v141 offset:57344
	v_mfma_f32_16x16x32_bf16 v[72:75], v[156:159], v[4:7], v[72:75]
	s_waitcnt lgkmcnt(11)
	v_mfma_f32_16x16x32_bf16 v[72:75], v[192:195], v[8:11], v[72:75]
	ds_read_b64_tr_b16 v[92:93], v140 offset:57344
	ds_read_b64_tr_b16 v[156:157], v136 offset:49152
	ds_read_b64_tr_b16 v[158:159], v137 offset:49152
	ds_read_b64_tr_b16 v[194:195], v137 offset:57344
	v_mfma_f32_16x16x32_bf16 v[76:79], v[200:203], v[12:15], v[72:75]
	v_mfma_f32_16x16x32_bf16 v[72:75], v[188:191], v[4:7], v[80:83]
	v_mfma_f32_16x16x32_bf16 v[72:75], v[196:199], v[8:11], v[72:75]
	v_mfma_f32_16x16x32_bf16 v[72:75], v[204:207], v[12:15], v[72:75]
	s_waitcnt lgkmcnt(11)
	v_mfma_f32_16x16x32_bf16 v[80:83], v[208:211], v[0:3], 0
	ds_read_b64_tr_b16 v[192:193], v136 offset:57344
	ds_read_b64_tr_b16 v[200:201], v138 offset:49152
	ds_read_b64_tr_b16 v[202:203], v142 offset:49152
	ds_read_b64_tr_b16 v[190:191], v142 offset:57344
	v_mfma_f32_16x16x32_bf16 v[80:83], v[216:219], v[4:7], v[80:83]
	s_waitcnt lgkmcnt(11)
	v_mfma_f32_16x16x32_bf16 v[80:83], v[224:227], v[8:11], v[80:83]
	ds_read_b64_tr_b16 v[188:189], v138 offset:57344
	ds_read_b64_tr_b16 v[196:197], v139 offset:49152
	ds_read_b64_tr_b16 v[198:199], v143 offset:49152
	ds_read_b64_tr_b16 v[206:207], v143 offset:57344
	v_mfma_f32_16x16x32_bf16 v[84:87], v[232:235], v[12:15], v[80:83]
	v_mfma_f32_16x16x32_bf16 v[80:83], v[212:215], v[0:3], 0
	v_mfma_f32_16x16x32_bf16 v[80:83], v[220:223], v[4:7], v[80:83]
	s_waitcnt lgkmcnt(10)
	v_mfma_f32_16x16x32_bf16 v[48:51], v[88:91], v[68:71], v[48:51]
	ds_read_b64_tr_b16 v[204:205], v139 offset:57344
	ds_read_b64_tr_b16 v[208:209], v145 offset:49152
	ds_read_b64_tr_b16 v[210:211], v146 offset:49152
	ds_read_b64_tr_b16 v[218:219], v146 offset:57344
	ds_read_b64_tr_b16 v[216:217], v145 offset:57344
	v_mfma_f32_16x16x32_bf16 v[48:51], v[92:95], v[64:67], v[48:51]
	s_waitcnt lgkmcnt(11)
	v_mfma_f32_16x16x32_bf16 v[40:43], v[156:159], v[68:71], v[40:43]
	ds_read_b64_tr_b16 v[224:225], v147 offset:49152
	ds_read_b64_tr_b16 v[226:227], v148 offset:49152
	ds_read_b64_tr_b16 v[234:235], v148 offset:57344
	ds_read_b64_tr_b16 v[232:233], v147 offset:57344
	v_mfma_f32_16x16x32_bf16 v[40:43], v[192:195], v[64:67], v[40:43]
	s_waitcnt lgkmcnt(11)
	v_mfma_f32_16x16x32_bf16 v[44:47], v[200:203], v[68:71], v[44:47]
	ds_read_b64_tr_b16 v[212:213], v149 offset:49152
	ds_read_b64_tr_b16 v[214:215], v150 offset:49152
	ds_read_b64_tr_b16 v[222:223], v150 offset:57344
	ds_read_b64_tr_b16 v[220:221], v149 offset:57344
	v_mfma_f32_16x16x32_bf16 v[44:47], v[188:191], v[64:67], v[44:47]
	s_waitcnt lgkmcnt(11)
	v_mfma_f32_16x16x32_bf16 v[56:59], v[196:199], v[68:71], v[56:59]
	ds_read_b64_tr_b16 v[88:89], v151 offset:49152
	ds_read_b64_tr_b16 v[90:91], v152 offset:49152
	ds_read_b64_tr_b16 v[94:95], v152 offset:57344
	ds_read_b64_tr_b16 v[92:93], v151 offset:57344
	v_mfma_f32_16x16x32_bf16 v[56:59], v[204:207], v[64:67], v[56:59]
	s_waitcnt lgkmcnt(11)
	v_mfma_f32_16x16x32_bf16 v[60:63], v[208:211], v[68:71], v[60:63]
	v_mfma_f32_16x16x32_bf16 v[60:63], v[216:219], v[64:67], v[60:63]
	s_waitcnt lgkmcnt(7)
	v_mfma_f32_16x16x32_bf16 v[52:55], v[224:227], v[68:71], v[52:55]
	v_mfma_f32_16x16x32_bf16 v[52:55], v[232:235], v[64:67], v[52:55]
	s_waitcnt lgkmcnt(3)
	v_mfma_f32_16x16x32_bf16 v[32:35], v[212:215], v[68:71], v[32:35]
	v_mfma_f32_16x16x32_bf16 v[32:35], v[220:223], v[64:67], v[32:35]
	v_mfma_f32_16x16x32_bf16 v[80:83], v[228:231], v[8:11], v[80:83]
	s_waitcnt lgkmcnt(0)
	v_mfma_f32_16x16x32_bf16 v[36:39], v[88:91], v[68:71], v[36:39]
	v_mfma_f32_16x16x32_bf16 v[80:83], v[236:239], v[12:15], v[80:83]
	v_mfma_f32_16x16x32_bf16 v[36:39], v[92:95], v[64:67], v[36:39]
	s_cbranch_vccnz .LBB0_641
	s_waitcnt vmcnt(3)
	ds_write_b128 v98, v[16:19] offset:16384
	s_waitcnt vmcnt(2)
	ds_write_b128 v99, v[20:23] offset:16384
	s_waitcnt vmcnt(1)
	ds_write_b128 v100, v[24:27] offset:32768
	s_waitcnt vmcnt(0)
	ds_write_b128 v124, v[28:31] offset:32768

.LBB0_663:
	ds_read_b128 v[176:179], v128 offset:16384
	ds_read_b128 v[180:183], v128 offset:17408
	ds_read_b128 v[188:191], v129 offset:16384
	ds_read_b128 v[192:195], v130 offset:16384
	ds_read_b128 v[196:199], v131 offset:16384
	ds_read_b128 v[200:203], v129 offset:17408
	ds_read_b128 v[204:207], v130 offset:17408
	ds_read_b128 v[208:211], v129 offset:24576
	ds_read_b128 v[212:215], v131 offset:17408
	ds_read_b128 v[216:219], v128 offset:24576
	ds_read_b128 v[220:223], v130 offset:24576
	ds_read_b128 v[224:227], v128 offset:25600
	ds_read_b128 v[228:231], v131 offset:24576
	ds_read_b128 v[232:235], v129 offset:25600
	ds_read_b128 v[236:239], v130 offset:25600
	v_pk_mul_f32 v[184:185], v[66:67], v[68:69]
	s_waitcnt lgkmcnt(11)
	v_mfma_f32_16x16x32_bf16 v[160:163], v[176:179], v[0:3], 0
	ds_read_b128 v[176:179], v131 offset:25600
	v_mul_f32_e32 v70, v70, v71
	v_mul_f32_e32 v157, v70, v157
	v_mul_f32_e32 v159, v157, v159
	v_mfma_f32_16x16x32_bf16 v[164:167], v[180:183], v[0:3], 0
	ds_read_b64_tr_b16 v[180:181], v140 offset:32768
	ds_read_b64_tr_b16 v[182:183], v141 offset:32768
	v_mul_f32_e32 v186, v153, v159
	v_pk_mul_f32 v[64:65], v[64:65], v[96:97]
	v_pk_mul_f32 v[72:73], v[72:73], v[74:75]
	v_mfma_f32_16x16x32_bf16 v[160:163], v[188:191], v[4:7], v[160:163]
	ds_read_b64_tr_b16 v[190:191], v141 offset:40960
	v_pk_mul_f32 v[96:97], v[64:65], v[186:187] op_sel_hi:[1,0]
	v_pk_mul_f32 v[84:85], v[84:85], v[94:95]
	v_mfma_f32_16x16x32_bf16 v[66:69], v[192:195], v[8:11], v[160:163]
	v_cvt_pk_bf16_f32 v173, v96, v97
	v_pk_mul_f32 v[96:97], v[76:77], v[78:79]
	s_waitcnt lgkmcnt(11)
	v_mfma_f32_16x16x32_bf16 v[68:71], v[196:199], v[12:15], v[66:69]
	ds_read_b64_tr_b16 v[188:189], v140 offset:40960
	ds_read_b64_tr_b16 v[192:193], v136 offset:32768
	ds_read_b64_tr_b16 v[194:195], v137 offset:32768
	ds_read_b64_tr_b16 v[198:199], v137 offset:40960
	v_pk_mul_f32 v[96:97], v[96:97], v[186:187] op_sel_hi:[1,0]
	v_pk_mul_f32 v[86:87], v[86:87], v[92:93]
	v_mfma_f32_16x16x32_bf16 v[164:167], v[200:203], v[4:7], v[164:167]
	v_mul_f32_e64 v66, v184, v186
	v_mul_f32_e64 v67, v185, v186
	v_pk_mul_f32 v[80:81], v[80:81], v[82:83]
	v_cvt_pk_bf16_f32 v172, v66, v67
	v_mfma_f32_16x16x32_bf16 v[64:67], v[204:207], v[8:11], v[164:167]
	s_and_b64 vcc, exec, s[10:11]
	s_waitcnt lgkmcnt(11)
	v_mfma_f32_16x16x32_bf16 v[64:67], v[212:215], v[12:15], v[64:67]
	ds_read_b64_tr_b16 v[196:197], v136 offset:40960
	ds_read_b64_tr_b16 v[200:201], v138 offset:32768
	ds_read_b64_tr_b16 v[202:203], v142 offset:32768
	ds_read_b64_tr_b16 v[206:207], v142 offset:40960
	v_mfma_f32_16x16x32_bf16 v[168:171], v[216:219], v[0:3], 0
	v_cvt_pk_bf16_f32 v174, v96, v97
	v_pk_mul_f32 v[96:97], v[72:73], v[186:187] op_sel_hi:[1,0]
	v_mfma_f32_16x16x32_bf16 v[76:79], v[208:211], v[4:7], v[168:171]
	v_cvt_pk_bf16_f32 v175, v96, v97
	v_mfma_f32_16x16x32_bf16 v[94:97], v[224:227], v[0:3], 0
	v_mfma_f32_16x16x32_bf16 v[72:75], v[220:223], v[8:11], v[76:79]
	v_mul_f32_e32 v162, v153, v158
	v_pk_mul_f32 v[84:85], v[84:85], v[162:163] op_sel_hi:[1,0]
	v_pk_mul_f32 v[86:87], v[86:87], v[162:163] op_sel_hi:[1,0]
	s_waitcnt lgkmcnt(10)
	v_mfma_f32_16x16x32_bf16 v[92:95], v[232:235], v[4:7], v[94:97]
	ds_read_b64_tr_b16 v[204:205], v138 offset:40960
	ds_read_b64_tr_b16 v[212:213], v139 offset:32768
	ds_read_b64_tr_b16 v[214:215], v143 offset:32768
	ds_read_b64_tr_b16 v[218:219], v143 offset:40960
	ds_read_b64_tr_b16 v[216:217], v139 offset:40960
	v_cvt_pk_bf16_f32 v84, v84, v85
	v_cvt_pk_bf16_f32 v85, v86, v87
	v_pk_mul_f32 v[86:87], v[88:89], v[90:91]
	v_mfma_f32_16x16x32_bf16 v[92:95], v[236:239], v[8:11], v[92:95]
	v_pk_mul_f32 v[86:87], v[86:87], v[162:163] op_sel_hi:[1,0]
	v_mfma_f32_16x16x32_bf16 v[76:79], v[176:179], v[12:15], v[92:95]
	v_cvt_pk_bf16_f32 v86, v86, v87
	s_nop 4
	v_pk_mul_f32 v[92:93], v[80:81], v[162:163] op_sel_hi:[1,0]
	s_waitcnt lgkmcnt(11)
	v_mfma_f32_16x16x32_bf16 v[48:51], v[180:183], v[172:175], v[48:51]
	ds_read_b64_tr_b16 v[208:209], v145 offset:32768
	ds_read_b64_tr_b16 v[210:211], v146 offset:32768
	ds_read_b64_tr_b16 v[226:227], v146 offset:40960
	ds_read_b64_tr_b16 v[224:225], v145 offset:40960
	v_cvt_pk_bf16_f32 v87, v92, v93
	s_waitcnt lgkmcnt(11)
	v_mfma_f32_16x16x32_bf16 v[40:43], v[192:195], v[172:175], v[40:43]
	ds_read_b64_tr_b16 v[220:221], v147 offset:32768
	ds_read_b64_tr_b16 v[222:223], v148 offset:32768
	ds_read_b64_tr_b16 v[234:235], v148 offset:40960
	ds_read_b64_tr_b16 v[232:233], v147 offset:40960
	v_mfma_f32_16x16x32_bf16 v[40:43], v[196:199], v[84:87], v[40:43]
	s_waitcnt lgkmcnt(11)
	v_mfma_f32_16x16x32_bf16 v[44:47], v[200:203], v[172:175], v[44:47]
	ds_read_b64_tr_b16 v[236:237], v149 offset:32768
	ds_read_b64_tr_b16 v[238:239], v150 offset:32768
	ds_read_b64_tr_b16 v[178:179], v150 offset:40960
	ds_read_b64_tr_b16 v[176:177], v149 offset:40960
	v_mfma_f32_16x16x32_bf16 v[44:47], v[204:207], v[84:87], v[44:47]
	s_waitcnt lgkmcnt(11)
	v_mfma_f32_16x16x32_bf16 v[56:59], v[212:215], v[172:175], v[56:59]
	ds_read_b64_tr_b16 v[180:181], v151 offset:32768
	ds_read_b64_tr_b16 v[182:183], v152 offset:32768
	ds_read_b64_tr_b16 v[194:195], v152 offset:40960
	ds_read_b64_tr_b16 v[192:193], v151 offset:40960
	v_mfma_f32_16x16x32_bf16 v[56:59], v[216:219], v[84:87], v[56:59]
	s_waitcnt lgkmcnt(11)
	v_mfma_f32_16x16x32_bf16 v[60:63], v[208:211], v[172:175], v[60:63]
	v_mfma_f32_16x16x32_bf16 v[60:63], v[224:227], v[84:87], v[60:63]
	s_waitcnt lgkmcnt(7)
	v_mfma_f32_16x16x32_bf16 v[52:55], v[220:223], v[172:175], v[52:55]
	v_mfma_f32_16x16x32_bf16 v[52:55], v[232:235], v[84:87], v[52:55]
	s_waitcnt lgkmcnt(3)
	v_mfma_f32_16x16x32_bf16 v[32:35], v[236:239], v[172:175], v[32:35]
	v_mfma_f32_16x16x32_bf16 v[32:35], v[176:179], v[84:87], v[32:35]
	s_waitcnt lgkmcnt(0)
	v_mfma_f32_16x16x32_bf16 v[36:39], v[180:183], v[172:175], v[36:39]
	v_mfma_f32_16x16x32_bf16 v[72:75], v[228:231], v[12:15], v[72:75]
	v_mfma_f32_16x16x32_bf16 v[48:51], v[188:191], v[84:87], v[48:51]
	v_mfma_f32_16x16x32_bf16 v[36:39], v[192:195], v[84:87], v[36:39]
	s_cbranch_vccnz .LBB0_665
	s_waitcnt vmcnt(3)
	ds_write_b128 v98, v[16:19]
	s_waitcnt vmcnt(2)
	ds_write_b128 v99, v[20:23]
	s_waitcnt vmcnt(1)
	ds_write_b128 v100, v[24:27] offset:49152
	s_waitcnt vmcnt(0)
	ds_write_b128 v124, v[28:31] offset:49152

.LBB0_742:
	ds_read_b128 v[88:91], v128
	ds_read_b128 v[92:95], v128 offset:1024
	ds_read_b128 v[156:159], v129
	ds_read_b128 v[188:191], v129 offset:1024
	ds_read_b128 v[192:195], v130
	ds_read_b128 v[196:199], v130 offset:1024
	ds_read_b128 v[200:203], v131
	ds_read_b128 v[204:207], v131 offset:1024
	ds_read_b128 v[208:211], v128 offset:8192
	ds_read_b128 v[212:215], v128 offset:9216
	ds_read_b128 v[216:219], v129 offset:8192
	ds_read_b128 v[220:223], v129 offset:9216
	ds_read_b128 v[224:227], v130 offset:8192
	ds_read_b128 v[228:231], v130 offset:9216
	ds_read_b128 v[232:235], v131 offset:8192
	s_and_b64 vcc, exec, s[10:11]
	s_waitcnt lgkmcnt(11)
	v_mfma_f32_16x16x32_bf16 v[72:75], v[88:91], v[0:3], 0
	ds_read_b128 v[236:239], v131 offset:9216
	ds_read_b64_tr_b16 v[88:89], v142 offset:49152
	ds_read_b64_tr_b16 v[90:91], v143 offset:49152
	v_mfma_f32_16x16x32_bf16 v[80:83], v[92:95], v[0:3], 0
	ds_read_b64_tr_b16 v[94:95], v143 offset:57344
	v_mfma_f32_16x16x32_bf16 v[72:75], v[156:159], v[4:7], v[72:75]
	s_waitcnt lgkmcnt(11)
	v_mfma_f32_16x16x32_bf16 v[72:75], v[192:195], v[8:11], v[72:75]
	ds_read_b64_tr_b16 v[92:93], v142 offset:57344
	ds_read_b64_tr_b16 v[156:157], v136 offset:49152
	ds_read_b64_tr_b16 v[158:159], v139 offset:49152
	ds_read_b64_tr_b16 v[194:195], v139 offset:57344
	v_mfma_f32_16x16x32_bf16 v[76:79], v[200:203], v[12:15], v[72:75]
	v_mfma_f32_16x16x32_bf16 v[72:75], v[188:191], v[4:7], v[80:83]
	v_mfma_f32_16x16x32_bf16 v[72:75], v[196:199], v[8:11], v[72:75]
	v_mfma_f32_16x16x32_bf16 v[72:75], v[204:207], v[12:15], v[72:75]
	s_waitcnt lgkmcnt(11)
	v_mfma_f32_16x16x32_bf16 v[80:83], v[208:211], v[0:3], 0
	ds_read_b64_tr_b16 v[192:193], v136 offset:57344
	ds_read_b64_tr_b16 v[200:201], v138 offset:49152
	ds_read_b64_tr_b16 v[202:203], v141 offset:49152
	ds_read_b64_tr_b16 v[190:191], v141 offset:57344
	v_mfma_f32_16x16x32_bf16 v[80:83], v[216:219], v[4:7], v[80:83]
	s_waitcnt lgkmcnt(11)
	v_mfma_f32_16x16x32_bf16 v[80:83], v[224:227], v[8:11], v[80:83]
	ds_read_b64_tr_b16 v[188:189], v138 offset:57344
	ds_read_b64_tr_b16 v[196:197], v137 offset:49152
	ds_read_b64_tr_b16 v[198:199], v140 offset:49152
	ds_read_b64_tr_b16 v[206:207], v140 offset:57344
	v_mfma_f32_16x16x32_bf16 v[84:87], v[232:235], v[12:15], v[80:83]
	v_mfma_f32_16x16x32_bf16 v[80:83], v[212:215], v[0:3], 0
	v_mfma_f32_16x16x32_bf16 v[80:83], v[220:223], v[4:7], v[80:83]
	s_waitcnt lgkmcnt(10)
	v_mfma_f32_16x16x32_bf16 v[60:63], v[88:91], v[64:67], v[60:63]
	ds_read_b64_tr_b16 v[204:205], v137 offset:57344
	ds_read_b64_tr_b16 v[208:209], v145 offset:49152
	ds_read_b64_tr_b16 v[210:211], v146 offset:49152
	ds_read_b64_tr_b16 v[218:219], v146 offset:57344
	ds_read_b64_tr_b16 v[216:217], v145 offset:57344
	v_mfma_f32_16x16x32_bf16 v[60:63], v[92:95], v[68:71], v[60:63]
	s_waitcnt lgkmcnt(11)
	v_mfma_f32_16x16x32_bf16 v[52:55], v[156:159], v[64:67], v[52:55]
	ds_read_b64_tr_b16 v[224:225], v147 offset:49152
	ds_read_b64_tr_b16 v[226:227], v148 offset:49152
	ds_read_b64_tr_b16 v[234:235], v148 offset:57344
	ds_read_b64_tr_b16 v[232:233], v147 offset:57344
	v_mfma_f32_16x16x32_bf16 v[52:55], v[192:195], v[68:71], v[52:55]
	s_waitcnt lgkmcnt(11)
	v_mfma_f32_16x16x32_bf16 v[44:47], v[200:203], v[64:67], v[44:47]
	ds_read_b64_tr_b16 v[212:213], v149 offset:49152
	ds_read_b64_tr_b16 v[214:215], v150 offset:49152
	ds_read_b64_tr_b16 v[222:223], v150 offset:57344
	ds_read_b64_tr_b16 v[220:221], v149 offset:57344
	v_mfma_f32_16x16x32_bf16 v[44:47], v[188:191], v[68:71], v[44:47]
	s_waitcnt lgkmcnt(11)
	v_mfma_f32_16x16x32_bf16 v[56:59], v[196:199], v[64:67], v[56:59]
	ds_read_b64_tr_b16 v[88:89], v151 offset:49152
	ds_read_b64_tr_b16 v[90:91], v152 offset:49152
	ds_read_b64_tr_b16 v[94:95], v152 offset:57344
	ds_read_b64_tr_b16 v[92:93], v151 offset:57344
	v_mfma_f32_16x16x32_bf16 v[56:59], v[204:207], v[68:71], v[56:59]
	s_waitcnt lgkmcnt(11)
	v_mfma_f32_16x16x32_bf16 v[48:51], v[208:211], v[64:67], v[48:51]
	v_mfma_f32_16x16x32_bf16 v[48:51], v[216:219], v[68:71], v[48:51]
	s_waitcnt lgkmcnt(7)
	v_mfma_f32_16x16x32_bf16 v[40:43], v[224:227], v[64:67], v[40:43]
	v_mfma_f32_16x16x32_bf16 v[40:43], v[232:235], v[68:71], v[40:43]
	s_waitcnt lgkmcnt(3)
	v_mfma_f32_16x16x32_bf16 v[32:35], v[212:215], v[64:67], v[32:35]
	v_mfma_f32_16x16x32_bf16 v[32:35], v[220:223], v[68:71], v[32:35]
	v_mfma_f32_16x16x32_bf16 v[80:83], v[228:231], v[8:11], v[80:83]
	s_waitcnt lgkmcnt(0)
	v_mfma_f32_16x16x32_bf16 v[36:39], v[88:91], v[64:67], v[36:39]
	v_mfma_f32_16x16x32_bf16 v[80:83], v[236:239], v[12:15], v[80:83]
	v_mfma_f32_16x16x32_bf16 v[36:39], v[92:95], v[68:71], v[36:39]
	s_cbranch_vccnz .LBB0_744
	s_waitcnt vmcnt(3)
	ds_write_b128 v98, v[16:19] offset:16384
	s_waitcnt vmcnt(2)
	ds_write_b128 v99, v[20:23] offset:16384
	s_waitcnt vmcnt(1)
	ds_write_b128 v100, v[24:27] offset:32768
	s_waitcnt vmcnt(0)
	ds_write_b128 v124, v[28:31] offset:32768

.LBB0_766:
	ds_read_b128 v[176:179], v128 offset:16384
	ds_read_b128 v[180:183], v128 offset:17408
	ds_read_b128 v[188:191], v129 offset:16384
	ds_read_b128 v[192:195], v130 offset:16384
	ds_read_b128 v[196:199], v131 offset:16384
	ds_read_b128 v[200:203], v129 offset:17408
	ds_read_b128 v[204:207], v130 offset:17408
	ds_read_b128 v[208:211], v129 offset:24576
	ds_read_b128 v[212:215], v131 offset:17408
	ds_read_b128 v[216:219], v128 offset:24576
	ds_read_b128 v[220:223], v130 offset:24576
	ds_read_b128 v[224:227], v128 offset:25600
	ds_read_b128 v[228:231], v131 offset:24576
	ds_read_b128 v[232:235], v129 offset:25600
	ds_read_b128 v[236:239], v130 offset:25600
	v_pk_mul_f32 v[184:185], v[66:67], v[68:69]
	s_waitcnt lgkmcnt(11)
	v_mfma_f32_16x16x32_bf16 v[160:163], v[176:179], v[0:3], 0
	ds_read_b128 v[176:179], v131 offset:25600
	v_mul_f32_e32 v70, v70, v71
	v_mul_f32_e32 v157, v70, v157
	v_mul_f32_e32 v159, v157, v159
	v_mfma_f32_16x16x32_bf16 v[164:167], v[180:183], v[0:3], 0
	ds_read_b64_tr_b16 v[180:181], v142 offset:32768
	ds_read_b64_tr_b16 v[182:183], v143 offset:32768
	v_mul_f32_e32 v186, v153, v159
	v_pk_mul_f32 v[64:65], v[64:65], v[96:97]
	v_pk_mul_f32 v[72:73], v[72:73], v[74:75]
	v_mfma_f32_16x16x32_bf16 v[160:163], v[188:191], v[4:7], v[160:163]
	ds_read_b64_tr_b16 v[190:191], v143 offset:40960
	v_pk_mul_f32 v[96:97], v[64:65], v[186:187] op_sel_hi:[1,0]
	v_pk_mul_f32 v[84:85], v[84:85], v[94:95]
	v_mfma_f32_16x16x32_bf16 v[66:69], v[192:195], v[8:11], v[160:163]
	v_cvt_pk_bf16_f32 v173, v96, v97
	v_pk_mul_f32 v[96:97], v[76:77], v[78:79]
	s_waitcnt lgkmcnt(11)
	v_mfma_f32_16x16x32_bf16 v[68:71], v[196:199], v[12:15], v[66:69]
	ds_read_b64_tr_b16 v[188:189], v142 offset:40960
	ds_read_b64_tr_b16 v[192:193], v136 offset:32768
	ds_read_b64_tr_b16 v[194:195], v139 offset:32768
	ds_read_b64_tr_b16 v[198:199], v139 offset:40960
	v_pk_mul_f32 v[96:97], v[96:97], v[186:187] op_sel_hi:[1,0]
	v_pk_mul_f32 v[86:87], v[86:87], v[92:93]
	v_mfma_f32_16x16x32_bf16 v[164:167], v[200:203], v[4:7], v[164:167]
	v_mul_f32_e64 v66, v184, v186
	v_mul_f32_e64 v67, v185, v186
	v_pk_mul_f32 v[80:81], v[80:81], v[82:83]
	v_cvt_pk_bf16_f32 v172, v66, v67
	v_mfma_f32_16x16x32_bf16 v[64:67], v[204:207], v[8:11], v[164:167]
	s_and_b64 vcc, exec, s[10:11]
	s_waitcnt lgkmcnt(11)
	v_mfma_f32_16x16x32_bf16 v[64:67], v[212:215], v[12:15], v[64:67]
	ds_read_b64_tr_b16 v[196:197], v136 offset:40960
	ds_read_b64_tr_b16 v[200:201], v138 offset:32768
	ds_read_b64_tr_b16 v[202:203], v141 offset:32768
	ds_read_b64_tr_b16 v[206:207], v141 offset:40960
	v_mfma_f32_16x16x32_bf16 v[168:171], v[216:219], v[0:3], 0
	v_cvt_pk_bf16_f32 v174, v96, v97
	v_pk_mul_f32 v[96:97], v[72:73], v[186:187] op_sel_hi:[1,0]
	v_mfma_f32_16x16x32_bf16 v[76:79], v[208:211], v[4:7], v[168:171]
	v_cvt_pk_bf16_f32 v175, v96, v97
	v_mfma_f32_16x16x32_bf16 v[94:97], v[224:227], v[0:3], 0
	v_mfma_f32_16x16x32_bf16 v[72:75], v[220:223], v[8:11], v[76:79]
	v_mul_f32_e32 v162, v153, v158
	v_pk_mul_f32 v[84:85], v[84:85], v[162:163] op_sel_hi:[1,0]
	v_pk_mul_f32 v[86:87], v[86:87], v[162:163] op_sel_hi:[1,0]
	s_waitcnt lgkmcnt(10)
	v_mfma_f32_16x16x32_bf16 v[92:95], v[232:235], v[4:7], v[94:97]
	ds_read_b64_tr_b16 v[204:205], v138 offset:40960
	ds_read_b64_tr_b16 v[212:213], v137 offset:32768
	ds_read_b64_tr_b16 v[214:215], v140 offset:32768
	ds_read_b64_tr_b16 v[218:219], v140 offset:40960
	ds_read_b64_tr_b16 v[216:217], v137 offset:40960
	v_cvt_pk_bf16_f32 v84, v84, v85
	v_cvt_pk_bf16_f32 v85, v86, v87
	v_pk_mul_f32 v[86:87], v[88:89], v[90:91]
	v_mfma_f32_16x16x32_bf16 v[92:95], v[236:239], v[8:11], v[92:95]
	v_pk_mul_f32 v[86:87], v[86:87], v[162:163] op_sel_hi:[1,0]
	v_mfma_f32_16x16x32_bf16 v[76:79], v[176:179], v[12:15], v[92:95]
	v_cvt_pk_bf16_f32 v86, v86, v87
	s_nop 4
	v_pk_mul_f32 v[92:93], v[80:81], v[162:163] op_sel_hi:[1,0]
	s_waitcnt lgkmcnt(11)
	v_mfma_f32_16x16x32_bf16 v[60:63], v[180:183], v[172:175], v[60:63]
	ds_read_b64_tr_b16 v[208:209], v145 offset:32768
	ds_read_b64_tr_b16 v[210:211], v146 offset:32768
	ds_read_b64_tr_b16 v[226:227], v146 offset:40960
	ds_read_b64_tr_b16 v[224:225], v145 offset:40960
	v_cvt_pk_bf16_f32 v87, v92, v93
	s_waitcnt lgkmcnt(11)
	v_mfma_f32_16x16x32_bf16 v[52:55], v[192:195], v[172:175], v[52:55]
	ds_read_b64_tr_b16 v[220:221], v147 offset:32768
	ds_read_b64_tr_b16 v[222:223], v148 offset:32768
	ds_read_b64_tr_b16 v[234:235], v148 offset:40960
	ds_read_b64_tr_b16 v[232:233], v147 offset:40960
	v_mfma_f32_16x16x32_bf16 v[52:55], v[196:199], v[84:87], v[52:55]
	s_waitcnt lgkmcnt(11)
	v_mfma_f32_16x16x32_bf16 v[44:47], v[200:203], v[172:175], v[44:47]
	ds_read_b64_tr_b16 v[236:237], v149 offset:32768
	ds_read_b64_tr_b16 v[238:239], v150 offset:32768
	ds_read_b64_tr_b16 v[178:179], v150 offset:40960
	ds_read_b64_tr_b16 v[176:177], v149 offset:40960
	v_mfma_f32_16x16x32_bf16 v[44:47], v[204:207], v[84:87], v[44:47]
	s_waitcnt lgkmcnt(11)
	v_mfma_f32_16x16x32_bf16 v[56:59], v[212:215], v[172:175], v[56:59]
	ds_read_b64_tr_b16 v[180:181], v151 offset:32768
	ds_read_b64_tr_b16 v[182:183], v152 offset:32768
	ds_read_b64_tr_b16 v[194:195], v152 offset:40960
	ds_read_b64_tr_b16 v[192:193], v151 offset:40960
	v_mfma_f32_16x16x32_bf16 v[56:59], v[216:219], v[84:87], v[56:59]
	s_waitcnt lgkmcnt(11)
	v_mfma_f32_16x16x32_bf16 v[48:51], v[208:211], v[172:175], v[48:51]
	v_mfma_f32_16x16x32_bf16 v[48:51], v[224:227], v[84:87], v[48:51]
	s_waitcnt lgkmcnt(7)
	v_mfma_f32_16x16x32_bf16 v[40:43], v[220:223], v[172:175], v[40:43]
	v_mfma_f32_16x16x32_bf16 v[40:43], v[232:235], v[84:87], v[40:43]
	s_waitcnt lgkmcnt(3)
	v_mfma_f32_16x16x32_bf16 v[32:35], v[236:239], v[172:175], v[32:35]
	v_mfma_f32_16x16x32_bf16 v[32:35], v[176:179], v[84:87], v[32:35]
	s_waitcnt lgkmcnt(0)
	v_mfma_f32_16x16x32_bf16 v[36:39], v[180:183], v[172:175], v[36:39]
	v_mfma_f32_16x16x32_bf16 v[72:75], v[228:231], v[12:15], v[72:75]
	v_mfma_f32_16x16x32_bf16 v[60:63], v[188:191], v[84:87], v[60:63]
	v_mfma_f32_16x16x32_bf16 v[36:39], v[192:195], v[84:87], v[36:39]
	s_cbranch_vccnz .LBB0_768
	s_waitcnt vmcnt(3)
	ds_write_b128 v98, v[16:19]
	s_waitcnt vmcnt(2)
	ds_write_b128 v99, v[20:23]
	s_waitcnt vmcnt(1)
	ds_write_b128 v100, v[24:27] offset:49152
	s_waitcnt vmcnt(0)
	ds_write_b128 v124, v[28:31] offset:49152

.LBB0_1919:
	ds_read_b128 v[88:91], v129
	ds_read_b128 v[92:95], v129 offset:1024
	ds_read_b128 v[96:99], v130
	ds_read_b128 v[152:155], v130 offset:1024
	ds_read_b128 v[176:179], v131
	ds_read_b128 v[180:183], v131 offset:1024
	ds_read_b128 v[184:187], v132
	ds_read_b128 v[188:191], v132 offset:1024
	ds_read_b128 v[192:195], v129 offset:8192
	ds_read_b128 v[196:199], v129 offset:9216
	ds_read_b128 v[200:203], v130 offset:8192
	ds_read_b128 v[204:207], v130 offset:9216
	ds_read_b128 v[208:211], v131 offset:8192
	ds_read_b128 v[212:215], v131 offset:9216
	ds_read_b128 v[216:219], v132 offset:8192
	s_and_b64 vcc, exec, s[6:7]
	s_waitcnt lgkmcnt(11)
	v_mfma_f32_16x16x32_bf16 v[72:75], v[88:91], v[0:3], v[240:243]
	ds_read_b128 v[220:223], v132 offset:9216
	ds_read_b64_tr_b16 v[224:225], v142 offset:49152
	ds_read_b64_tr_b16 v[226:227], v146 offset:49152
	ds_read_b64_tr_b16 v[230:231], v146 offset:57344
	v_mfma_f32_16x16x32_bf16 v[72:75], v[96:99], v[4:7], v[72:75]
	v_mfma_f32_16x16x32_bf16 v[76:79], v[92:95], v[0:3], v[240:243]
	s_waitcnt lgkmcnt(11)
	v_mfma_f32_16x16x32_bf16 v[72:75], v[176:179], v[8:11], v[72:75]
	ds_read_b64_tr_b16 v[228:229], v142 offset:57344
	ds_read_b64_tr_b16 v[232:233], v136 offset:49152
	ds_read_b64_tr_b16 v[234:235], v137 offset:49152
	ds_read_b64_tr_b16 v[238:239], v137 offset:57344
	v_mfma_f32_16x16x32_bf16 v[84:87], v[184:187], v[12:15], v[72:75]
	v_mfma_f32_16x16x32_bf16 v[72:75], v[152:155], v[4:7], v[76:79]
	v_mfma_f32_16x16x32_bf16 v[72:75], v[180:183], v[8:11], v[72:75]
	v_mfma_f32_16x16x32_bf16 v[80:83], v[188:191], v[12:15], v[72:75]
	s_waitcnt lgkmcnt(11)
	s_nop 5
	v_mfma_f32_16x16x32_bf16 v[72:75], v[192:195], v[0:3], v[240:243]
	ds_read_b64_tr_b16 v[236:237], v136 offset:57344
	ds_read_b64_tr_b16 v[88:89], v139 offset:49152
	ds_read_b64_tr_b16 v[90:91], v145 offset:49152
	ds_read_b64_tr_b16 v[98:99], v145 offset:57344
	v_mfma_f32_16x16x32_bf16 v[72:75], v[200:203], v[4:7], v[72:75]
	s_waitcnt lgkmcnt(11)
	v_mfma_f32_16x16x32_bf16 v[72:75], v[208:211], v[8:11], v[72:75]
	ds_read_b64_tr_b16 v[96:97], v139 offset:57344
	ds_read_b64_tr_b16 v[92:93], v140 offset:49152
	ds_read_b64_tr_b16 v[94:95], v147 offset:49152
	ds_read_b64_tr_b16 v[178:179], v147 offset:57344
	v_mfma_f32_16x16x32_bf16 v[76:79], v[216:219], v[12:15], v[72:75]
	v_mfma_f32_16x16x32_bf16 v[72:75], v[196:199], v[0:3], v[240:243]
	v_mfma_f32_16x16x32_bf16 v[72:75], v[204:207], v[4:7], v[72:75]
	s_waitcnt lgkmcnt(10)
	v_mfma_f32_16x16x32_bf16 v[60:63], v[224:227], v[68:71], v[60:63]
	ds_read_b64_tr_b16 v[176:177], v140 offset:57344
	ds_read_b64_tr_b16 v[184:185], v148 offset:49152
	ds_read_b64_tr_b16 v[186:187], v149 offset:49152
	ds_read_b64_tr_b16 v[154:155], v149 offset:57344
	ds_read_b64_tr_b16 v[152:153], v148 offset:57344
	v_mfma_f32_16x16x32_bf16 v[60:63], v[228:231], v[64:67], v[60:63]
	s_waitcnt lgkmcnt(11)
	v_mfma_f32_16x16x32_bf16 v[52:55], v[232:235], v[68:71], v[52:55]
	ds_read_b64_tr_b16 v[180:181], v133 offset:49152
	ds_read_b64_tr_b16 v[182:183], v134 offset:49152
	ds_read_b64_tr_b16 v[190:191], v134 offset:57344
	ds_read_b64_tr_b16 v[188:189], v133 offset:57344
	v_mfma_f32_16x16x32_bf16 v[52:55], v[236:239], v[64:67], v[52:55]
	s_waitcnt lgkmcnt(11)
	v_mfma_f32_16x16x32_bf16 v[48:51], v[88:91], v[68:71], v[48:51]
	ds_read_b64_tr_b16 v[192:193], v135 offset:49152
	ds_read_b64_tr_b16 v[194:195], v138 offset:49152
	ds_read_b64_tr_b16 v[202:203], v138 offset:57344
	ds_read_b64_tr_b16 v[200:201], v135 offset:57344
	v_mfma_f32_16x16x32_bf16 v[48:51], v[96:99], v[64:67], v[48:51]
	s_waitcnt lgkmcnt(11)
	v_mfma_f32_16x16x32_bf16 v[56:59], v[92:95], v[68:71], v[56:59]
	ds_read_b64_tr_b16 v[208:209], v141 offset:49152
	ds_read_b64_tr_b16 v[210:211], v143 offset:49152
	ds_read_b64_tr_b16 v[218:219], v143 offset:57344
	ds_read_b64_tr_b16 v[216:217], v141 offset:57344
	v_mfma_f32_16x16x32_bf16 v[56:59], v[176:179], v[64:67], v[56:59]
	s_waitcnt lgkmcnt(11)
	v_mfma_f32_16x16x32_bf16 v[32:35], v[184:187], v[68:71], v[32:35]
	v_mfma_f32_16x16x32_bf16 v[32:35], v[152:155], v[64:67], v[32:35]
	s_waitcnt lgkmcnt(7)
	v_mfma_f32_16x16x32_bf16 v[36:39], v[180:183], v[68:71], v[36:39]
	v_mfma_f32_16x16x32_bf16 v[36:39], v[188:191], v[64:67], v[36:39]
	s_waitcnt lgkmcnt(3)
	v_mfma_f32_16x16x32_bf16 v[40:43], v[192:195], v[68:71], v[40:43]
	v_mfma_f32_16x16x32_bf16 v[40:43], v[200:203], v[64:67], v[40:43]
	v_mfma_f32_16x16x32_bf16 v[72:75], v[212:215], v[8:11], v[72:75]
	s_waitcnt lgkmcnt(0)
	v_mfma_f32_16x16x32_bf16 v[44:47], v[208:211], v[68:71], v[44:47]
	v_mfma_f32_16x16x32_bf16 v[72:75], v[220:223], v[12:15], v[72:75]
	v_mfma_f32_16x16x32_bf16 v[44:47], v[216:219], v[64:67], v[44:47]
	s_cbranch_vccnz .LBB0_1921
	v_add_u32_e32 v64, 0, v109
	s_waitcnt vmcnt(3)
	ds_write_b128 v100, v[16:19] offset:16384
	s_waitcnt vmcnt(2)
	ds_write_b128 v124, v[20:23] offset:16384
	s_waitcnt vmcnt(1)
	ds_write_b128 v64, v[24:27] offset:32768
	v_add_u32_e32 v64, 0, v112
	s_waitcnt vmcnt(0)
	ds_write_b128 v64, v[28:31] offset:32768

.LBB0_1927:
	ds_read_b128 v[168:171], v129 offset:16384
	ds_read_b128 v[172:175], v130 offset:16384
	ds_read_b128 v[176:179], v131 offset:16384
	ds_read_b128 v[180:183], v129 offset:17408
	ds_read_b128 v[184:187], v132 offset:16384
	ds_read_b128 v[188:191], v130 offset:17408
	ds_read_b128 v[192:195], v131 offset:17408
	ds_read_b128 v[196:199], v129 offset:24576
	ds_read_b128 v[200:203], v132 offset:17408
	ds_read_b128 v[204:207], v130 offset:24576
	ds_read_b128 v[208:211], v131 offset:24576
	ds_read_b128 v[212:215], v129 offset:25600
	ds_read_b128 v[216:219], v132 offset:24576
	ds_read_b128 v[220:223], v130 offset:25600
	ds_read_b128 v[224:227], v131 offset:25600
	v_sub_f32_e32 v64, v84, v96
	v_exp_f32_e32 v96, v64
	v_sub_f32_e32 v64, v85, v97
	v_exp_f32_e32 v97, v64
	v_sub_f32_e32 v64, v86, v98
	v_exp_f32_e32 v98, v64
	v_sub_f32_e32 v64, v87, v99
	v_exp_f32_e32 v99, v64
	v_sub_f32_e32 v64, v80, v92
	v_exp_f32_e32 v153, v64
	v_sub_f32_e32 v64, v81, v93
	v_exp_f32_e32 v154, v64
	v_sub_f32_e32 v64, v82, v94
	v_exp_f32_e32 v155, v64
	v_sub_f32_e32 v64, v83, v95
	s_waitcnt lgkmcnt(11)
	v_mfma_f32_16x16x32_bf16 v[84:87], v[168:171], v[0:3], v[240:243]
	ds_read_b128 v[228:231], v132 offset:25600
	ds_read_b64_tr_b16 v[232:233], v142 offset:32768
	ds_read_b64_tr_b16 v[234:235], v146 offset:32768
	ds_read_b64_tr_b16 v[238:239], v146 offset:40960
	v_exp_f32_e32 v156, v64
	v_sub_f32_e32 v64, v76, v88
	v_exp_f32_e32 v157, v64
	v_mfma_f32_16x16x32_bf16 v[92:95], v[180:183], v[0:3], v[240:243]
	v_sub_f32_e32 v64, v77, v89
	v_sub_f32_e32 v70, v73, v67
	v_mfma_f32_16x16x32_bf16 v[84:87], v[172:175], v[4:7], v[84:87]
	v_exp_f32_e32 v158, v64
	v_sub_f32_e32 v64, v78, v90
	v_exp_f32_e32 v159, v64
	v_sub_f32_e32 v64, v79, v91
	s_waitcnt lgkmcnt(10)
	v_mfma_f32_16x16x32_bf16 v[88:91], v[188:191], v[4:7], v[92:95]
	ds_read_b64_tr_b16 v[236:237], v142 offset:40960
	ds_read_b64_tr_b16 v[168:169], v136 offset:32768
	ds_read_b64_tr_b16 v[170:171], v137 offset:32768
	ds_read_b64_tr_b16 v[182:183], v137 offset:40960
	ds_read_b64_tr_b16 v[180:181], v136 offset:40960
	v_exp_f32_e32 v160, v64
	v_mfma_f32_16x16x32_bf16 v[80:83], v[176:179], v[8:11], v[84:87]
	v_sub_f32_e32 v64, v72, v66
	v_exp_f32_e32 v161, v64
	v_mfma_f32_16x16x32_bf16 v[76:79], v[192:195], v[8:11], v[88:91]
	v_sub_f32_e32 v68, v74, v68
	s_and_b64 vcc, exec, s[6:7]
	v_mfma_f32_16x16x32_bf16 v[92:95], v[196:199], v[0:3], v[240:243]
	v_mfma_f32_16x16x32_bf16 v[80:83], v[184:187], v[12:15], v[80:83]
	v_exp_f32_e32 v162, v70
	v_exp_f32_e32 v163, v68
	v_mfma_f32_16x16x32_bf16 v[76:79], v[200:203], v[12:15], v[76:79]
	s_waitcnt lgkmcnt(11)
	v_mfma_f32_16x16x32_bf16 v[88:91], v[204:207], v[4:7], v[92:95]
	ds_read_b64_tr_b16 v[172:173], v139 offset:32768
	ds_read_b64_tr_b16 v[174:175], v145 offset:32768
	ds_read_b64_tr_b16 v[190:191], v145 offset:40960
	ds_read_b64_tr_b16 v[188:189], v139 offset:40960
	v_sub_f32_e32 v68, v75, v69
	v_mfma_f32_16x16x32_bf16 v[84:87], v[208:211], v[8:11], v[88:91]
	v_cvt_pk_bf16_f32 v92, v96, v97
	v_cvt_pk_bf16_f32 v93, v98, v99
	v_cvt_pk_bf16_f32 v94, v153, v154
	v_mfma_f32_16x16x32_bf16 v[64:67], v[216:219], v[12:15], v[84:87]
	v_cvt_pk_bf16_f32 v95, v155, v156
	v_mfma_f32_16x16x32_bf16 v[84:87], v[212:215], v[0:3], v[240:243]
	v_exp_f32_e32 v164, v68
	s_waitcnt lgkmcnt(11)
	v_mfma_f32_16x16x32_bf16 v[84:87], v[220:223], v[4:7], v[84:87]
	ds_read_b64_tr_b16 v[176:177], v140 offset:32768
	ds_read_b64_tr_b16 v[178:179], v147 offset:32768
	ds_read_b64_tr_b16 v[194:195], v147 offset:40960
	ds_read_b64_tr_b16 v[192:193], v140 offset:40960
	v_mfma_f32_16x16x32_bf16 v[68:71], v[224:227], v[8:11], v[84:87]
	s_nop 2
	v_cvt_pk_bf16_f32 v84, v157, v158
	v_mfma_f32_16x16x32_bf16 v[68:71], v[228:231], v[12:15], v[68:71]
	v_cvt_pk_bf16_f32 v85, v159, v160
	v_cvt_pk_bf16_f32 v86, v161, v162
	s_waitcnt lgkmcnt(11)
	v_mfma_f32_16x16x32_bf16 v[60:63], v[232:235], v[92:95], v[60:63]
	ds_read_b64_tr_b16 v[196:197], v148 offset:32768
	ds_read_b64_tr_b16 v[198:199], v149 offset:32768
	ds_read_b64_tr_b16 v[186:187], v149 offset:40960
	ds_read_b64_tr_b16 v[184:185], v148 offset:40960
	v_cvt_pk_bf16_f32 v87, v163, v164
	s_nop 1
	v_mfma_f32_16x16x32_bf16 v[60:63], v[236:239], v[84:87], v[60:63]
	s_waitcnt lgkmcnt(11)
	v_mfma_f32_16x16x32_bf16 v[52:55], v[168:171], v[92:95], v[52:55]
	ds_read_b64_tr_b16 v[200:201], v133 offset:32768
	ds_read_b64_tr_b16 v[202:203], v134 offset:32768
	ds_read_b64_tr_b16 v[206:207], v134 offset:40960
	ds_read_b64_tr_b16 v[204:205], v133 offset:40960
	v_mfma_f32_16x16x32_bf16 v[52:55], v[180:183], v[84:87], v[52:55]
	s_waitcnt lgkmcnt(11)
	v_mfma_f32_16x16x32_bf16 v[48:51], v[172:175], v[92:95], v[48:51]
	ds_read_b64_tr_b16 v[208:209], v135 offset:32768
	ds_read_b64_tr_b16 v[210:211], v138 offset:32768
	ds_read_b64_tr_b16 v[218:219], v138 offset:40960
	ds_read_b64_tr_b16 v[216:217], v135 offset:40960
	v_mfma_f32_16x16x32_bf16 v[48:51], v[188:191], v[84:87], v[48:51]
	s_waitcnt lgkmcnt(11)
	v_mfma_f32_16x16x32_bf16 v[56:59], v[176:179], v[92:95], v[56:59]
	ds_read_b64_tr_b16 v[212:213], v141 offset:32768
	ds_read_b64_tr_b16 v[214:215], v143 offset:32768
	ds_read_b64_tr_b16 v[222:223], v143 offset:40960
	ds_read_b64_tr_b16 v[220:221], v141 offset:40960
	v_mfma_f32_16x16x32_bf16 v[56:59], v[192:195], v[84:87], v[56:59]
	s_waitcnt lgkmcnt(11)
	v_mfma_f32_16x16x32_bf16 v[32:35], v[196:199], v[92:95], v[32:35]
	v_mfma_f32_16x16x32_bf16 v[32:35], v[184:187], v[84:87], v[32:35]
	s_waitcnt lgkmcnt(7)
	v_mfma_f32_16x16x32_bf16 v[36:39], v[200:203], v[92:95], v[36:39]
	v_mfma_f32_16x16x32_bf16 v[36:39], v[204:207], v[84:87], v[36:39]
	s_waitcnt lgkmcnt(3)
	v_mfma_f32_16x16x32_bf16 v[40:43], v[208:211], v[92:95], v[40:43]
	v_mfma_f32_16x16x32_bf16 v[40:43], v[216:219], v[84:87], v[40:43]
	s_waitcnt lgkmcnt(0)
	v_mfma_f32_16x16x32_bf16 v[44:47], v[212:215], v[92:95], v[44:47]
	v_mfma_f32_16x16x32_bf16 v[44:47], v[220:223], v[84:87], v[44:47]
	s_cbranch_vccnz .LBB0_1929
	v_add_u32_e32 v72, 0, v109
	s_waitcnt vmcnt(3)
	ds_write_b128 v100, v[16:19]
	s_waitcnt vmcnt(2)
	ds_write_b128 v124, v[20:23]
	s_waitcnt vmcnt(1)
	ds_write_b128 v72, v[24:27] offset:49152
	v_add_u32_e32 v72, 0, v112
	s_waitcnt vmcnt(0)
	ds_write_b128 v72, v[28:31] offset:49152

.LBB0_1958:
	ds_read_b128 v[88:91], v129
	ds_read_b128 v[92:95], v129 offset:1024
	ds_read_b128 v[96:99], v130
	ds_read_b128 v[152:155], v130 offset:1024
	ds_read_b128 v[172:175], v131
	ds_read_b128 v[176:179], v131 offset:1024
	ds_read_b128 v[180:183], v132
	ds_read_b128 v[184:187], v132 offset:1024
	ds_read_b128 v[188:191], v129 offset:8192
	ds_read_b128 v[192:195], v129 offset:9216
	ds_read_b128 v[196:199], v130 offset:8192
	ds_read_b128 v[200:203], v130 offset:9216
	ds_read_b128 v[204:207], v131 offset:8192
	ds_read_b128 v[208:211], v131 offset:9216
	ds_read_b128 v[212:215], v132 offset:8192
	s_and_b64 vcc, exec, s[6:7]
	s_waitcnt lgkmcnt(11)
	v_mfma_f32_16x16x32_bf16 v[72:75], v[88:91], v[0:3], v[240:243]
	ds_read_b128 v[216:219], v132 offset:9216
	ds_read_b64_tr_b16 v[220:221], v146 offset:49152
	ds_read_b64_tr_b16 v[222:223], v148 offset:49152
	ds_read_b64_tr_b16 v[226:227], v148 offset:57344
	v_mfma_f32_16x16x32_bf16 v[72:75], v[96:99], v[4:7], v[72:75]
	v_mfma_f32_16x16x32_bf16 v[76:79], v[92:95], v[0:3], v[240:243]
	s_waitcnt lgkmcnt(11)
	v_mfma_f32_16x16x32_bf16 v[72:75], v[172:175], v[8:11], v[72:75]
	ds_read_b64_tr_b16 v[224:225], v146 offset:57344
	ds_read_b64_tr_b16 v[228:229], v139 offset:49152
	ds_read_b64_tr_b16 v[230:231], v142 offset:49152
	ds_read_b64_tr_b16 v[234:235], v142 offset:57344
	v_mfma_f32_16x16x32_bf16 v[84:87], v[180:183], v[12:15], v[72:75]
	v_mfma_f32_16x16x32_bf16 v[72:75], v[152:155], v[4:7], v[76:79]
	v_mfma_f32_16x16x32_bf16 v[72:75], v[176:179], v[8:11], v[72:75]
	v_mfma_f32_16x16x32_bf16 v[80:83], v[184:187], v[12:15], v[72:75]
	s_waitcnt lgkmcnt(11)
	s_nop 5
	v_mfma_f32_16x16x32_bf16 v[72:75], v[188:191], v[0:3], v[240:243]
	ds_read_b64_tr_b16 v[232:233], v139 offset:57344
	ds_read_b64_tr_b16 v[236:237], v141 offset:49152
	ds_read_b64_tr_b16 v[238:239], v145 offset:49152
	ds_read_b64_tr_b16 v[90:91], v145 offset:57344
	v_mfma_f32_16x16x32_bf16 v[72:75], v[196:199], v[4:7], v[72:75]
	s_waitcnt lgkmcnt(11)
	v_mfma_f32_16x16x32_bf16 v[72:75], v[204:207], v[8:11], v[72:75]
	ds_read_b64_tr_b16 v[88:89], v141 offset:57344
	ds_read_b64_tr_b16 v[96:97], v140 offset:49152
	ds_read_b64_tr_b16 v[98:99], v143 offset:49152
	ds_read_b64_tr_b16 v[94:95], v143 offset:57344
	v_mfma_f32_16x16x32_bf16 v[76:79], v[212:215], v[12:15], v[72:75]
	v_mfma_f32_16x16x32_bf16 v[72:75], v[192:195], v[0:3], v[240:243]
	v_mfma_f32_16x16x32_bf16 v[72:75], v[200:203], v[4:7], v[72:75]
	s_waitcnt lgkmcnt(10)
	v_mfma_f32_16x16x32_bf16 v[60:63], v[220:223], v[68:71], v[60:63]
	ds_read_b64_tr_b16 v[92:93], v140 offset:57344
	ds_read_b64_tr_b16 v[172:173], v147 offset:49152
	ds_read_b64_tr_b16 v[174:175], v149 offset:49152
	ds_read_b64_tr_b16 v[182:183], v149 offset:57344
	ds_read_b64_tr_b16 v[180:181], v147 offset:57344
	v_mfma_f32_16x16x32_bf16 v[60:63], v[224:227], v[64:67], v[60:63]
	s_waitcnt lgkmcnt(11)
	v_mfma_f32_16x16x32_bf16 v[56:59], v[228:231], v[68:71], v[56:59]
	ds_read_b64_tr_b16 v[152:153], v133 offset:49152
	ds_read_b64_tr_b16 v[154:155], v134 offset:49152
	ds_read_b64_tr_b16 v[178:179], v134 offset:57344
	ds_read_b64_tr_b16 v[176:177], v133 offset:57344
	v_mfma_f32_16x16x32_bf16 v[56:59], v[232:235], v[64:67], v[56:59]
	s_waitcnt lgkmcnt(11)
	v_mfma_f32_16x16x32_bf16 v[52:55], v[236:239], v[68:71], v[52:55]
	ds_read_b64_tr_b16 v[184:185], v135 offset:49152
	ds_read_b64_tr_b16 v[186:187], v136 offset:49152
	ds_read_b64_tr_b16 v[190:191], v136 offset:57344
	ds_read_b64_tr_b16 v[188:189], v135 offset:57344
	v_mfma_f32_16x16x32_bf16 v[52:55], v[88:91], v[64:67], v[52:55]
	s_waitcnt lgkmcnt(11)
	v_mfma_f32_16x16x32_bf16 v[48:51], v[96:99], v[68:71], v[48:51]
	ds_read_b64_tr_b16 v[196:197], v137 offset:49152
	ds_read_b64_tr_b16 v[198:199], v138 offset:49152
	ds_read_b64_tr_b16 v[206:207], v138 offset:57344
	ds_read_b64_tr_b16 v[204:205], v137 offset:57344
	v_mfma_f32_16x16x32_bf16 v[48:51], v[92:95], v[64:67], v[48:51]
	s_waitcnt lgkmcnt(11)
	v_mfma_f32_16x16x32_bf16 v[32:35], v[172:175], v[68:71], v[32:35]
	v_mfma_f32_16x16x32_bf16 v[32:35], v[180:183], v[64:67], v[32:35]
	s_waitcnt lgkmcnt(7)
	v_mfma_f32_16x16x32_bf16 v[36:39], v[152:155], v[68:71], v[36:39]
	v_mfma_f32_16x16x32_bf16 v[36:39], v[176:179], v[64:67], v[36:39]
	s_waitcnt lgkmcnt(3)
	v_mfma_f32_16x16x32_bf16 v[40:43], v[184:187], v[68:71], v[40:43]
	v_mfma_f32_16x16x32_bf16 v[40:43], v[188:191], v[64:67], v[40:43]
	v_mfma_f32_16x16x32_bf16 v[72:75], v[208:211], v[8:11], v[72:75]
	s_waitcnt lgkmcnt(0)
	v_mfma_f32_16x16x32_bf16 v[44:47], v[196:199], v[68:71], v[44:47]
	v_mfma_f32_16x16x32_bf16 v[72:75], v[216:219], v[12:15], v[72:75]
	v_mfma_f32_16x16x32_bf16 v[44:47], v[204:207], v[64:67], v[44:47]
	s_cbranch_vccnz .LBB0_1960
	v_add_u32_e32 v64, 0, v109
	s_waitcnt vmcnt(3)
	ds_write_b128 v100, v[16:19] offset:16384
	s_waitcnt vmcnt(2)
	ds_write_b128 v124, v[20:23] offset:16384
	s_waitcnt vmcnt(1)
	ds_write_b128 v64, v[24:27] offset:32768
	v_add_u32_e32 v64, 0, v112
	s_waitcnt vmcnt(0)
	ds_write_b128 v64, v[28:31] offset:32768

.LBB0_1966:
	ds_read_b128 v[164:167], v129 offset:16384
	ds_read_b128 v[168:171], v130 offset:16384
	ds_read_b128 v[172:175], v131 offset:16384
	ds_read_b128 v[176:179], v129 offset:17408
	ds_read_b128 v[180:183], v132 offset:16384
	ds_read_b128 v[184:187], v130 offset:17408
	ds_read_b128 v[188:191], v131 offset:17408
	ds_read_b128 v[192:195], v129 offset:24576
	ds_read_b128 v[196:199], v132 offset:17408
	ds_read_b128 v[200:203], v130 offset:24576
	ds_read_b128 v[204:207], v131 offset:24576
	ds_read_b128 v[208:211], v129 offset:25600
	ds_read_b128 v[212:215], v132 offset:24576
	ds_read_b128 v[216:219], v130 offset:25600
	ds_read_b128 v[220:223], v131 offset:25600
	v_sub_f32_e32 v64, v84, v96
	v_exp_f32_e32 v96, v64
	v_sub_f32_e32 v64, v85, v97
	v_exp_f32_e32 v97, v64
	v_sub_f32_e32 v64, v86, v98
	v_exp_f32_e32 v98, v64
	v_sub_f32_e32 v64, v87, v99
	v_exp_f32_e32 v99, v64
	v_sub_f32_e32 v64, v80, v92
	v_exp_f32_e32 v152, v64
	v_sub_f32_e32 v64, v81, v93
	v_exp_f32_e32 v153, v64
	v_sub_f32_e32 v64, v82, v94
	v_exp_f32_e32 v154, v64
	v_sub_f32_e32 v64, v83, v95
	s_waitcnt lgkmcnt(11)
	v_mfma_f32_16x16x32_bf16 v[84:87], v[164:167], v[0:3], v[240:243]
	ds_read_b128 v[224:227], v132 offset:25600
	ds_read_b64_tr_b16 v[228:229], v146 offset:32768
	ds_read_b64_tr_b16 v[230:231], v148 offset:32768
	ds_read_b64_tr_b16 v[234:235], v148 offset:40960
	v_exp_f32_e32 v155, v64
	v_sub_f32_e32 v64, v76, v88
	v_mfma_f32_16x16x32_bf16 v[84:87], v[168:171], v[4:7], v[84:87]
	v_exp_f32_e32 v156, v64
	v_sub_f32_e32 v64, v77, v89
	v_mfma_f32_16x16x32_bf16 v[92:95], v[176:179], v[0:3], v[240:243]
	v_exp_f32_e32 v157, v64
	v_sub_f32_e32 v64, v78, v90
	v_exp_f32_e32 v158, v64
	v_sub_f32_e32 v64, v79, v91
	s_waitcnt lgkmcnt(10)
	v_mfma_f32_16x16x32_bf16 v[88:91], v[184:187], v[4:7], v[92:95]
	ds_read_b64_tr_b16 v[232:233], v146 offset:40960
	ds_read_b64_tr_b16 v[236:237], v139 offset:32768
	ds_read_b64_tr_b16 v[238:239], v142 offset:32768
	ds_read_b64_tr_b16 v[166:167], v142 offset:40960
	ds_read_b64_tr_b16 v[164:165], v139 offset:40960
	v_exp_f32_e32 v159, v64
	v_mfma_f32_16x16x32_bf16 v[80:83], v[172:175], v[8:11], v[84:87]
	v_sub_f32_e32 v64, v72, v66
	v_sub_f32_e32 v70, v73, v67
	v_mfma_f32_16x16x32_bf16 v[76:79], v[188:191], v[8:11], v[88:91]
	v_sub_f32_e32 v68, v74, v68
	s_and_b64 vcc, exec, s[6:7]
	v_mfma_f32_16x16x32_bf16 v[92:95], v[192:195], v[0:3], v[240:243]
	v_mfma_f32_16x16x32_bf16 v[76:79], v[196:199], v[12:15], v[76:79]
	s_waitcnt lgkmcnt(11)
	v_mfma_f32_16x16x32_bf16 v[88:91], v[200:203], v[4:7], v[92:95]
	ds_read_b64_tr_b16 v[168:169], v141 offset:32768
	ds_read_b64_tr_b16 v[170:171], v145 offset:32768
	ds_read_b64_tr_b16 v[178:179], v145 offset:40960
	ds_read_b64_tr_b16 v[176:177], v141 offset:40960
	v_mfma_f32_16x16x32_bf16 v[80:83], v[180:183], v[12:15], v[80:83]
	v_exp_f32_e32 v160, v64
	v_exp_f32_e32 v161, v70
	v_mfma_f32_16x16x32_bf16 v[84:87], v[204:207], v[8:11], v[88:91]
	v_exp_f32_e32 v162, v68
	v_mfma_f32_16x16x32_bf16 v[64:67], v[212:215], v[12:15], v[84:87]
	v_sub_f32_e32 v68, v75, v69
	v_exp_f32_e32 v163, v68
	v_mfma_f32_16x16x32_bf16 v[84:87], v[208:211], v[0:3], v[240:243]
	v_cvt_pk_bf16_f32 v92, v96, v97
	v_cvt_pk_bf16_f32 v93, v98, v99
	s_waitcnt lgkmcnt(11)
	v_mfma_f32_16x16x32_bf16 v[84:87], v[216:219], v[4:7], v[84:87]
	ds_read_b64_tr_b16 v[184:185], v140 offset:32768
	ds_read_b64_tr_b16 v[186:187], v143 offset:32768
	ds_read_b64_tr_b16 v[174:175], v143 offset:40960
	ds_read_b64_tr_b16 v[172:173], v140 offset:40960
	v_cvt_pk_bf16_f32 v94, v152, v153
	v_cvt_pk_bf16_f32 v95, v154, v155
	v_mfma_f32_16x16x32_bf16 v[68:71], v[220:223], v[8:11], v[84:87]
	s_nop 2
	v_cvt_pk_bf16_f32 v84, v156, v157
	v_mfma_f32_16x16x32_bf16 v[68:71], v[224:227], v[12:15], v[68:71]
	v_cvt_pk_bf16_f32 v85, v158, v159
	v_cvt_pk_bf16_f32 v86, v160, v161
	s_waitcnt lgkmcnt(11)
	v_mfma_f32_16x16x32_bf16 v[60:63], v[228:231], v[92:95], v[60:63]
	ds_read_b64_tr_b16 v[188:189], v147 offset:32768
	ds_read_b64_tr_b16 v[190:191], v149 offset:32768
	ds_read_b64_tr_b16 v[194:195], v149 offset:40960
	ds_read_b64_tr_b16 v[192:193], v147 offset:40960
	v_cvt_pk_bf16_f32 v87, v162, v163
	s_nop 1
	v_mfma_f32_16x16x32_bf16 v[60:63], v[232:235], v[84:87], v[60:63]
	s_waitcnt lgkmcnt(11)
	v_mfma_f32_16x16x32_bf16 v[56:59], v[236:239], v[92:95], v[56:59]
	ds_read_b64_tr_b16 v[196:197], v133 offset:32768
	ds_read_b64_tr_b16 v[198:199], v134 offset:32768
	ds_read_b64_tr_b16 v[202:203], v134 offset:40960
	ds_read_b64_tr_b16 v[200:201], v133 offset:40960
	v_mfma_f32_16x16x32_bf16 v[56:59], v[164:167], v[84:87], v[56:59]
	s_waitcnt lgkmcnt(11)
	v_mfma_f32_16x16x32_bf16 v[52:55], v[168:171], v[92:95], v[52:55]
	ds_read_b64_tr_b16 v[180:181], v135 offset:32768
	ds_read_b64_tr_b16 v[182:183], v136 offset:32768
	ds_read_b64_tr_b16 v[206:207], v136 offset:40960
	ds_read_b64_tr_b16 v[204:205], v135 offset:40960
	v_mfma_f32_16x16x32_bf16 v[52:55], v[176:179], v[84:87], v[52:55]
	s_waitcnt lgkmcnt(11)
	v_mfma_f32_16x16x32_bf16 v[48:51], v[184:187], v[92:95], v[48:51]
	ds_read_b64_tr_b16 v[212:213], v137 offset:32768
	ds_read_b64_tr_b16 v[214:215], v138 offset:32768
	ds_read_b64_tr_b16 v[210:211], v138 offset:40960
	ds_read_b64_tr_b16 v[208:209], v137 offset:40960
	v_mfma_f32_16x16x32_bf16 v[48:51], v[172:175], v[84:87], v[48:51]
	s_waitcnt lgkmcnt(11)
	v_mfma_f32_16x16x32_bf16 v[32:35], v[188:191], v[92:95], v[32:35]
	v_mfma_f32_16x16x32_bf16 v[32:35], v[192:195], v[84:87], v[32:35]
	s_waitcnt lgkmcnt(7)
	v_mfma_f32_16x16x32_bf16 v[36:39], v[196:199], v[92:95], v[36:39]
	v_mfma_f32_16x16x32_bf16 v[36:39], v[200:203], v[84:87], v[36:39]
	s_waitcnt lgkmcnt(3)
	v_mfma_f32_16x16x32_bf16 v[40:43], v[180:183], v[92:95], v[40:43]
	v_mfma_f32_16x16x32_bf16 v[40:43], v[204:207], v[84:87], v[40:43]
	s_waitcnt lgkmcnt(0)
	v_mfma_f32_16x16x32_bf16 v[44:47], v[212:215], v[92:95], v[44:47]
	v_mfma_f32_16x16x32_bf16 v[44:47], v[208:211], v[84:87], v[44:47]
	s_cbranch_vccnz .LBB0_1968
	v_add_u32_e32 v72, 0, v109
	s_waitcnt vmcnt(3)
	ds_write_b128 v100, v[16:19]
	s_waitcnt vmcnt(2)
	ds_write_b128 v124, v[20:23]
	s_waitcnt vmcnt(1)
	ds_write_b128 v72, v[24:27] offset:49152
	v_add_u32_e32 v72, 0, v112
	s_waitcnt vmcnt(0)
	ds_write_b128 v72, v[28:31] offset:49152

.LBB0_2030:
	ds_read_b128 v[88:91], v128
	ds_read_b128 v[92:95], v128 offset:1024
	ds_read_b128 v[156:159], v129
	ds_read_b128 v[188:191], v129 offset:1024
	ds_read_b128 v[192:195], v130
	ds_read_b128 v[196:199], v130 offset:1024
	ds_read_b128 v[200:203], v131
	ds_read_b128 v[204:207], v131 offset:1024
	ds_read_b128 v[208:211], v128 offset:8192
	ds_read_b128 v[212:215], v128 offset:9216
	ds_read_b128 v[216:219], v129 offset:8192
	ds_read_b128 v[220:223], v129 offset:9216
	ds_read_b128 v[224:227], v130 offset:8192
	ds_read_b128 v[228:231], v130 offset:9216
	ds_read_b128 v[232:235], v131 offset:8192
	s_and_b64 vcc, exec, s[6:7]
	s_waitcnt lgkmcnt(11)
	v_mfma_f32_16x16x32_bf16 v[72:75], v[88:91], v[0:3], 0
	ds_read_b128 v[236:239], v131 offset:9216
	ds_read_b64_tr_b16 v[88:89], v140 offset:49152
	ds_read_b64_tr_b16 v[90:91], v141 offset:49152
	v_mfma_f32_16x16x32_bf16 v[80:83], v[92:95], v[0:3], 0
	ds_read_b64_tr_b16 v[94:95], v141 offset:57344
	v_mfma_f32_16x16x32_bf16 v[72:75], v[156:159], v[4:7], v[72:75]
	s_waitcnt lgkmcnt(11)
	v_mfma_f32_16x16x32_bf16 v[72:75], v[192:195], v[8:11], v[72:75]
	ds_read_b64_tr_b16 v[92:93], v140 offset:57344
	ds_read_b64_tr_b16 v[156:157], v136 offset:49152
	ds_read_b64_tr_b16 v[158:159], v137 offset:49152
	ds_read_b64_tr_b16 v[194:195], v137 offset:57344
	v_mfma_f32_16x16x32_bf16 v[76:79], v[200:203], v[12:15], v[72:75]
	v_mfma_f32_16x16x32_bf16 v[72:75], v[188:191], v[4:7], v[80:83]
	v_mfma_f32_16x16x32_bf16 v[72:75], v[196:199], v[8:11], v[72:75]
	v_mfma_f32_16x16x32_bf16 v[72:75], v[204:207], v[12:15], v[72:75]
	s_waitcnt lgkmcnt(11)
	v_mfma_f32_16x16x32_bf16 v[80:83], v[208:211], v[0:3], 0
	ds_read_b64_tr_b16 v[192:193], v136 offset:57344
	ds_read_b64_tr_b16 v[200:201], v138 offset:49152
	ds_read_b64_tr_b16 v[202:203], v142 offset:49152
	ds_read_b64_tr_b16 v[190:191], v142 offset:57344
	v_mfma_f32_16x16x32_bf16 v[80:83], v[216:219], v[4:7], v[80:83]
	s_waitcnt lgkmcnt(11)
	v_mfma_f32_16x16x32_bf16 v[80:83], v[224:227], v[8:11], v[80:83]
	ds_read_b64_tr_b16 v[188:189], v138 offset:57344
	ds_read_b64_tr_b16 v[196:197], v139 offset:49152
	ds_read_b64_tr_b16 v[198:199], v143 offset:49152
	ds_read_b64_tr_b16 v[206:207], v143 offset:57344
	v_mfma_f32_16x16x32_bf16 v[84:87], v[232:235], v[12:15], v[80:83]
	v_mfma_f32_16x16x32_bf16 v[80:83], v[212:215], v[0:3], 0
	v_mfma_f32_16x16x32_bf16 v[80:83], v[220:223], v[4:7], v[80:83]
	s_waitcnt lgkmcnt(10)
	v_mfma_f32_16x16x32_bf16 v[48:51], v[88:91], v[68:71], v[48:51]
	ds_read_b64_tr_b16 v[204:205], v139 offset:57344
	ds_read_b64_tr_b16 v[208:209], v145 offset:49152
	ds_read_b64_tr_b16 v[210:211], v146 offset:49152
	ds_read_b64_tr_b16 v[218:219], v146 offset:57344
	ds_read_b64_tr_b16 v[216:217], v145 offset:57344
	v_mfma_f32_16x16x32_bf16 v[48:51], v[92:95], v[64:67], v[48:51]
	s_waitcnt lgkmcnt(11)
	v_mfma_f32_16x16x32_bf16 v[40:43], v[156:159], v[68:71], v[40:43]
	ds_read_b64_tr_b16 v[224:225], v147 offset:49152
	ds_read_b64_tr_b16 v[226:227], v148 offset:49152
	ds_read_b64_tr_b16 v[234:235], v148 offset:57344
	ds_read_b64_tr_b16 v[232:233], v147 offset:57344
	v_mfma_f32_16x16x32_bf16 v[40:43], v[192:195], v[64:67], v[40:43]
	s_waitcnt lgkmcnt(11)
	v_mfma_f32_16x16x32_bf16 v[44:47], v[200:203], v[68:71], v[44:47]
	ds_read_b64_tr_b16 v[212:213], v149 offset:49152
	ds_read_b64_tr_b16 v[214:215], v150 offset:49152
	ds_read_b64_tr_b16 v[222:223], v150 offset:57344
	ds_read_b64_tr_b16 v[220:221], v149 offset:57344
	v_mfma_f32_16x16x32_bf16 v[44:47], v[188:191], v[64:67], v[44:47]
	s_waitcnt lgkmcnt(11)
	v_mfma_f32_16x16x32_bf16 v[56:59], v[196:199], v[68:71], v[56:59]
	ds_read_b64_tr_b16 v[88:89], v151 offset:49152
	ds_read_b64_tr_b16 v[90:91], v152 offset:49152
	ds_read_b64_tr_b16 v[94:95], v152 offset:57344
	ds_read_b64_tr_b16 v[92:93], v151 offset:57344
	v_mfma_f32_16x16x32_bf16 v[56:59], v[204:207], v[64:67], v[56:59]
	s_waitcnt lgkmcnt(11)
	v_mfma_f32_16x16x32_bf16 v[60:63], v[208:211], v[68:71], v[60:63]
	v_mfma_f32_16x16x32_bf16 v[60:63], v[216:219], v[64:67], v[60:63]
	s_waitcnt lgkmcnt(7)
	v_mfma_f32_16x16x32_bf16 v[52:55], v[224:227], v[68:71], v[52:55]
	v_mfma_f32_16x16x32_bf16 v[52:55], v[232:235], v[64:67], v[52:55]
	s_waitcnt lgkmcnt(3)
	v_mfma_f32_16x16x32_bf16 v[32:35], v[212:215], v[68:71], v[32:35]
	v_mfma_f32_16x16x32_bf16 v[32:35], v[220:223], v[64:67], v[32:35]
	v_mfma_f32_16x16x32_bf16 v[80:83], v[228:231], v[8:11], v[80:83]
	s_waitcnt lgkmcnt(0)
	v_mfma_f32_16x16x32_bf16 v[36:39], v[88:91], v[68:71], v[36:39]
	v_mfma_f32_16x16x32_bf16 v[80:83], v[236:239], v[12:15], v[80:83]
	v_mfma_f32_16x16x32_bf16 v[36:39], v[92:95], v[64:67], v[36:39]
	s_cbranch_vccnz .LBB0_2032
	s_waitcnt vmcnt(3)
	ds_write_b128 v98, v[16:19] offset:16384
	s_waitcnt vmcnt(2)
	ds_write_b128 v99, v[20:23] offset:16384
	s_waitcnt vmcnt(1)
	ds_write_b128 v100, v[24:27] offset:32768
	s_waitcnt vmcnt(0)
	ds_write_b128 v124, v[28:31] offset:32768

.LBB0_2054:
	ds_read_b128 v[176:179], v128 offset:16384
	ds_read_b128 v[180:183], v128 offset:17408
	ds_read_b128 v[188:191], v129 offset:16384
	ds_read_b128 v[192:195], v130 offset:16384
	ds_read_b128 v[196:199], v131 offset:16384
	ds_read_b128 v[200:203], v129 offset:17408
	ds_read_b128 v[204:207], v130 offset:17408
	ds_read_b128 v[208:211], v129 offset:24576
	ds_read_b128 v[212:215], v131 offset:17408
	ds_read_b128 v[216:219], v128 offset:24576
	ds_read_b128 v[220:223], v130 offset:24576
	ds_read_b128 v[224:227], v128 offset:25600
	ds_read_b128 v[228:231], v131 offset:24576
	ds_read_b128 v[232:235], v129 offset:25600
	ds_read_b128 v[236:239], v130 offset:25600
	v_pk_mul_f32 v[184:185], v[66:67], v[68:69]
	s_waitcnt lgkmcnt(11)
	v_mfma_f32_16x16x32_bf16 v[160:163], v[176:179], v[0:3], 0
	ds_read_b128 v[176:179], v131 offset:25600
	v_mul_f32_e32 v70, v70, v71
	v_mul_f32_e32 v157, v70, v157
	v_mul_f32_e32 v159, v157, v159
	v_mfma_f32_16x16x32_bf16 v[164:167], v[180:183], v[0:3], 0
	ds_read_b64_tr_b16 v[180:181], v140 offset:32768
	ds_read_b64_tr_b16 v[182:183], v141 offset:32768
	v_mul_f32_e32 v186, v153, v159
	v_pk_mul_f32 v[64:65], v[64:65], v[96:97]
	v_pk_mul_f32 v[72:73], v[72:73], v[74:75]
	v_mfma_f32_16x16x32_bf16 v[160:163], v[188:191], v[4:7], v[160:163]
	ds_read_b64_tr_b16 v[190:191], v141 offset:40960
	v_pk_mul_f32 v[96:97], v[64:65], v[186:187] op_sel_hi:[1,0]
	v_pk_mul_f32 v[84:85], v[84:85], v[94:95]
	v_mfma_f32_16x16x32_bf16 v[66:69], v[192:195], v[8:11], v[160:163]
	v_cvt_pk_bf16_f32 v173, v96, v97
	v_pk_mul_f32 v[96:97], v[76:77], v[78:79]
	s_waitcnt lgkmcnt(11)
	v_mfma_f32_16x16x32_bf16 v[68:71], v[196:199], v[12:15], v[66:69]
	ds_read_b64_tr_b16 v[188:189], v140 offset:40960
	ds_read_b64_tr_b16 v[192:193], v136 offset:32768
	ds_read_b64_tr_b16 v[194:195], v137 offset:32768
	ds_read_b64_tr_b16 v[198:199], v137 offset:40960
	v_pk_mul_f32 v[96:97], v[96:97], v[186:187] op_sel_hi:[1,0]
	v_pk_mul_f32 v[86:87], v[86:87], v[92:93]
	v_mfma_f32_16x16x32_bf16 v[164:167], v[200:203], v[4:7], v[164:167]
	v_mul_f32_e64 v66, v184, v186
	v_mul_f32_e64 v67, v185, v186
	v_pk_mul_f32 v[80:81], v[80:81], v[82:83]
	v_cvt_pk_bf16_f32 v172, v66, v67
	v_mfma_f32_16x16x32_bf16 v[64:67], v[204:207], v[8:11], v[164:167]
	s_and_b64 vcc, exec, s[6:7]
	s_waitcnt lgkmcnt(11)
	v_mfma_f32_16x16x32_bf16 v[64:67], v[212:215], v[12:15], v[64:67]
	ds_read_b64_tr_b16 v[196:197], v136 offset:40960
	ds_read_b64_tr_b16 v[200:201], v138 offset:32768
	ds_read_b64_tr_b16 v[202:203], v142 offset:32768
	ds_read_b64_tr_b16 v[206:207], v142 offset:40960
	v_mfma_f32_16x16x32_bf16 v[168:171], v[216:219], v[0:3], 0
	v_cvt_pk_bf16_f32 v174, v96, v97
	v_pk_mul_f32 v[96:97], v[72:73], v[186:187] op_sel_hi:[1,0]
	v_mfma_f32_16x16x32_bf16 v[76:79], v[208:211], v[4:7], v[168:171]
	v_cvt_pk_bf16_f32 v175, v96, v97
	v_mfma_f32_16x16x32_bf16 v[94:97], v[224:227], v[0:3], 0
	v_mfma_f32_16x16x32_bf16 v[72:75], v[220:223], v[8:11], v[76:79]
	v_mul_f32_e32 v162, v153, v158
	v_pk_mul_f32 v[84:85], v[84:85], v[162:163] op_sel_hi:[1,0]
	v_pk_mul_f32 v[86:87], v[86:87], v[162:163] op_sel_hi:[1,0]
	s_waitcnt lgkmcnt(10)
	v_mfma_f32_16x16x32_bf16 v[92:95], v[232:235], v[4:7], v[94:97]
	ds_read_b64_tr_b16 v[204:205], v138 offset:40960
	ds_read_b64_tr_b16 v[212:213], v139 offset:32768
	ds_read_b64_tr_b16 v[214:215], v143 offset:32768
	ds_read_b64_tr_b16 v[218:219], v143 offset:40960
	ds_read_b64_tr_b16 v[216:217], v139 offset:40960
	v_cvt_pk_bf16_f32 v84, v84, v85
	v_cvt_pk_bf16_f32 v85, v86, v87
	v_pk_mul_f32 v[86:87], v[88:89], v[90:91]
	v_mfma_f32_16x16x32_bf16 v[92:95], v[236:239], v[8:11], v[92:95]
	v_pk_mul_f32 v[86:87], v[86:87], v[162:163] op_sel_hi:[1,0]
	v_mfma_f32_16x16x32_bf16 v[76:79], v[176:179], v[12:15], v[92:95]
	v_cvt_pk_bf16_f32 v86, v86, v87
	s_nop 4
	v_pk_mul_f32 v[92:93], v[80:81], v[162:163] op_sel_hi:[1,0]
	s_waitcnt lgkmcnt(11)
	v_mfma_f32_16x16x32_bf16 v[48:51], v[180:183], v[172:175], v[48:51]
	ds_read_b64_tr_b16 v[208:209], v145 offset:32768
	ds_read_b64_tr_b16 v[210:211], v146 offset:32768
	ds_read_b64_tr_b16 v[226:227], v146 offset:40960
	ds_read_b64_tr_b16 v[224:225], v145 offset:40960
	v_cvt_pk_bf16_f32 v87, v92, v93
	s_waitcnt lgkmcnt(11)
	v_mfma_f32_16x16x32_bf16 v[40:43], v[192:195], v[172:175], v[40:43]
	ds_read_b64_tr_b16 v[220:221], v147 offset:32768
	ds_read_b64_tr_b16 v[222:223], v148 offset:32768
	ds_read_b64_tr_b16 v[234:235], v148 offset:40960
	ds_read_b64_tr_b16 v[232:233], v147 offset:40960
	v_mfma_f32_16x16x32_bf16 v[40:43], v[196:199], v[84:87], v[40:43]
	s_waitcnt lgkmcnt(11)
	v_mfma_f32_16x16x32_bf16 v[44:47], v[200:203], v[172:175], v[44:47]
	ds_read_b64_tr_b16 v[236:237], v149 offset:32768
	ds_read_b64_tr_b16 v[238:239], v150 offset:32768
	ds_read_b64_tr_b16 v[178:179], v150 offset:40960
	ds_read_b64_tr_b16 v[176:177], v149 offset:40960
	v_mfma_f32_16x16x32_bf16 v[44:47], v[204:207], v[84:87], v[44:47]
	s_waitcnt lgkmcnt(11)
	v_mfma_f32_16x16x32_bf16 v[56:59], v[212:215], v[172:175], v[56:59]
	ds_read_b64_tr_b16 v[180:181], v151 offset:32768
	ds_read_b64_tr_b16 v[182:183], v152 offset:32768
	ds_read_b64_tr_b16 v[194:195], v152 offset:40960
	ds_read_b64_tr_b16 v[192:193], v151 offset:40960
	v_mfma_f32_16x16x32_bf16 v[56:59], v[216:219], v[84:87], v[56:59]
	s_waitcnt lgkmcnt(11)
	v_mfma_f32_16x16x32_bf16 v[60:63], v[208:211], v[172:175], v[60:63]
	v_mfma_f32_16x16x32_bf16 v[60:63], v[224:227], v[84:87], v[60:63]
	s_waitcnt lgkmcnt(7)
	v_mfma_f32_16x16x32_bf16 v[52:55], v[220:223], v[172:175], v[52:55]
	v_mfma_f32_16x16x32_bf16 v[52:55], v[232:235], v[84:87], v[52:55]
	s_waitcnt lgkmcnt(3)
	v_mfma_f32_16x16x32_bf16 v[32:35], v[236:239], v[172:175], v[32:35]
	v_mfma_f32_16x16x32_bf16 v[32:35], v[176:179], v[84:87], v[32:35]
	s_waitcnt lgkmcnt(0)
	v_mfma_f32_16x16x32_bf16 v[36:39], v[180:183], v[172:175], v[36:39]
	v_mfma_f32_16x16x32_bf16 v[72:75], v[228:231], v[12:15], v[72:75]
	v_mfma_f32_16x16x32_bf16 v[48:51], v[188:191], v[84:87], v[48:51]
	v_mfma_f32_16x16x32_bf16 v[36:39], v[192:195], v[84:87], v[36:39]
	s_cbranch_vccnz .LBB0_2056
	s_waitcnt vmcnt(3)
	ds_write_b128 v98, v[16:19]
	s_waitcnt vmcnt(2)
	ds_write_b128 v99, v[20:23]
	s_waitcnt vmcnt(1)
	ds_write_b128 v100, v[24:27] offset:49152
	s_waitcnt vmcnt(0)
	ds_write_b128 v124, v[28:31] offset:49152

.LBB0_2133:
	ds_read_b128 v[88:91], v128
	ds_read_b128 v[92:95], v128 offset:1024
	ds_read_b128 v[156:159], v129
	ds_read_b128 v[188:191], v129 offset:1024
	ds_read_b128 v[192:195], v130
	ds_read_b128 v[196:199], v130 offset:1024
	ds_read_b128 v[200:203], v131
	ds_read_b128 v[204:207], v131 offset:1024
	ds_read_b128 v[208:211], v128 offset:8192
	ds_read_b128 v[212:215], v128 offset:9216
	ds_read_b128 v[216:219], v129 offset:8192
	ds_read_b128 v[220:223], v129 offset:9216
	ds_read_b128 v[224:227], v130 offset:8192
	ds_read_b128 v[228:231], v130 offset:9216
	ds_read_b128 v[232:235], v131 offset:8192
	s_and_b64 vcc, exec, s[6:7]
	s_waitcnt lgkmcnt(11)
	v_mfma_f32_16x16x32_bf16 v[72:75], v[88:91], v[0:3], 0
	ds_read_b128 v[236:239], v131 offset:9216
	ds_read_b64_tr_b16 v[88:89], v142 offset:49152
	ds_read_b64_tr_b16 v[90:91], v143 offset:49152
	v_mfma_f32_16x16x32_bf16 v[80:83], v[92:95], v[0:3], 0
	ds_read_b64_tr_b16 v[94:95], v143 offset:57344
	v_mfma_f32_16x16x32_bf16 v[72:75], v[156:159], v[4:7], v[72:75]
	s_waitcnt lgkmcnt(11)
	v_mfma_f32_16x16x32_bf16 v[72:75], v[192:195], v[8:11], v[72:75]
	ds_read_b64_tr_b16 v[92:93], v142 offset:57344
	ds_read_b64_tr_b16 v[156:157], v136 offset:49152
	ds_read_b64_tr_b16 v[158:159], v139 offset:49152
	ds_read_b64_tr_b16 v[194:195], v139 offset:57344
	v_mfma_f32_16x16x32_bf16 v[76:79], v[200:203], v[12:15], v[72:75]
	v_mfma_f32_16x16x32_bf16 v[72:75], v[188:191], v[4:7], v[80:83]
	v_mfma_f32_16x16x32_bf16 v[72:75], v[196:199], v[8:11], v[72:75]
	v_mfma_f32_16x16x32_bf16 v[72:75], v[204:207], v[12:15], v[72:75]
	s_waitcnt lgkmcnt(11)
	v_mfma_f32_16x16x32_bf16 v[80:83], v[208:211], v[0:3], 0
	ds_read_b64_tr_b16 v[192:193], v136 offset:57344
	ds_read_b64_tr_b16 v[200:201], v138 offset:49152
	ds_read_b64_tr_b16 v[202:203], v141 offset:49152
	ds_read_b64_tr_b16 v[190:191], v141 offset:57344
	v_mfma_f32_16x16x32_bf16 v[80:83], v[216:219], v[4:7], v[80:83]
	s_waitcnt lgkmcnt(11)
	v_mfma_f32_16x16x32_bf16 v[80:83], v[224:227], v[8:11], v[80:83]
	ds_read_b64_tr_b16 v[188:189], v138 offset:57344
	ds_read_b64_tr_b16 v[196:197], v137 offset:49152
	ds_read_b64_tr_b16 v[198:199], v140 offset:49152
	ds_read_b64_tr_b16 v[206:207], v140 offset:57344
	v_mfma_f32_16x16x32_bf16 v[84:87], v[232:235], v[12:15], v[80:83]
	v_mfma_f32_16x16x32_bf16 v[80:83], v[212:215], v[0:3], 0
	v_mfma_f32_16x16x32_bf16 v[80:83], v[220:223], v[4:7], v[80:83]
	s_waitcnt lgkmcnt(10)
	v_mfma_f32_16x16x32_bf16 v[60:63], v[88:91], v[64:67], v[60:63]
	ds_read_b64_tr_b16 v[204:205], v137 offset:57344
	ds_read_b64_tr_b16 v[208:209], v145 offset:49152
	ds_read_b64_tr_b16 v[210:211], v146 offset:49152
	ds_read_b64_tr_b16 v[218:219], v146 offset:57344
	ds_read_b64_tr_b16 v[216:217], v145 offset:57344
	v_mfma_f32_16x16x32_bf16 v[60:63], v[92:95], v[68:71], v[60:63]
	s_waitcnt lgkmcnt(11)
	v_mfma_f32_16x16x32_bf16 v[52:55], v[156:159], v[64:67], v[52:55]
	ds_read_b64_tr_b16 v[224:225], v147 offset:49152
	ds_read_b64_tr_b16 v[226:227], v148 offset:49152
	ds_read_b64_tr_b16 v[234:235], v148 offset:57344
	ds_read_b64_tr_b16 v[232:233], v147 offset:57344
	v_mfma_f32_16x16x32_bf16 v[52:55], v[192:195], v[68:71], v[52:55]
	s_waitcnt lgkmcnt(11)
	v_mfma_f32_16x16x32_bf16 v[44:47], v[200:203], v[64:67], v[44:47]
	ds_read_b64_tr_b16 v[212:213], v149 offset:49152
	ds_read_b64_tr_b16 v[214:215], v150 offset:49152
	ds_read_b64_tr_b16 v[222:223], v150 offset:57344
	ds_read_b64_tr_b16 v[220:221], v149 offset:57344
	v_mfma_f32_16x16x32_bf16 v[44:47], v[188:191], v[68:71], v[44:47]
	s_waitcnt lgkmcnt(11)
	v_mfma_f32_16x16x32_bf16 v[56:59], v[196:199], v[64:67], v[56:59]
	ds_read_b64_tr_b16 v[88:89], v151 offset:49152
	ds_read_b64_tr_b16 v[90:91], v152 offset:49152
	ds_read_b64_tr_b16 v[94:95], v152 offset:57344
	ds_read_b64_tr_b16 v[92:93], v151 offset:57344
	v_mfma_f32_16x16x32_bf16 v[56:59], v[204:207], v[68:71], v[56:59]
	s_waitcnt lgkmcnt(11)
	v_mfma_f32_16x16x32_bf16 v[48:51], v[208:211], v[64:67], v[48:51]
	v_mfma_f32_16x16x32_bf16 v[48:51], v[216:219], v[68:71], v[48:51]
	s_waitcnt lgkmcnt(7)
	v_mfma_f32_16x16x32_bf16 v[40:43], v[224:227], v[64:67], v[40:43]
	v_mfma_f32_16x16x32_bf16 v[40:43], v[232:235], v[68:71], v[40:43]
	s_waitcnt lgkmcnt(3)
	v_mfma_f32_16x16x32_bf16 v[32:35], v[212:215], v[64:67], v[32:35]
	v_mfma_f32_16x16x32_bf16 v[32:35], v[220:223], v[68:71], v[32:35]
	v_mfma_f32_16x16x32_bf16 v[80:83], v[228:231], v[8:11], v[80:83]
	s_waitcnt lgkmcnt(0)
	v_mfma_f32_16x16x32_bf16 v[36:39], v[88:91], v[64:67], v[36:39]
	v_mfma_f32_16x16x32_bf16 v[80:83], v[236:239], v[12:15], v[80:83]
	v_mfma_f32_16x16x32_bf16 v[36:39], v[92:95], v[68:71], v[36:39]
	s_cbranch_vccnz .LBB0_2135
	s_waitcnt vmcnt(3)
	ds_write_b128 v98, v[16:19] offset:16384
	s_waitcnt vmcnt(2)
	ds_write_b128 v99, v[20:23] offset:16384
	s_waitcnt vmcnt(1)
	ds_write_b128 v100, v[24:27] offset:32768
	s_waitcnt vmcnt(0)
	ds_write_b128 v124, v[28:31] offset:32768

.LBB0_2157:
	ds_read_b128 v[176:179], v128 offset:16384
	ds_read_b128 v[180:183], v128 offset:17408
	ds_read_b128 v[188:191], v129 offset:16384
	ds_read_b128 v[192:195], v130 offset:16384
	ds_read_b128 v[196:199], v131 offset:16384
	ds_read_b128 v[200:203], v129 offset:17408
	ds_read_b128 v[204:207], v130 offset:17408
	ds_read_b128 v[208:211], v129 offset:24576
	ds_read_b128 v[212:215], v131 offset:17408
	ds_read_b128 v[216:219], v128 offset:24576
	ds_read_b128 v[220:223], v130 offset:24576
	ds_read_b128 v[224:227], v128 offset:25600
	ds_read_b128 v[228:231], v131 offset:24576
	ds_read_b128 v[232:235], v129 offset:25600
	ds_read_b128 v[236:239], v130 offset:25600
	v_pk_mul_f32 v[184:185], v[66:67], v[68:69]
	s_waitcnt lgkmcnt(11)
	v_mfma_f32_16x16x32_bf16 v[160:163], v[176:179], v[0:3], 0
	ds_read_b128 v[176:179], v131 offset:25600
	v_mul_f32_e32 v70, v70, v71
	v_mul_f32_e32 v157, v70, v157
	v_mul_f32_e32 v159, v157, v159
	v_mfma_f32_16x16x32_bf16 v[164:167], v[180:183], v[0:3], 0
	ds_read_b64_tr_b16 v[180:181], v142 offset:32768
	ds_read_b64_tr_b16 v[182:183], v143 offset:32768
	v_mul_f32_e32 v186, v153, v159
	v_pk_mul_f32 v[64:65], v[64:65], v[96:97]
	v_pk_mul_f32 v[72:73], v[72:73], v[74:75]
	v_mfma_f32_16x16x32_bf16 v[160:163], v[188:191], v[4:7], v[160:163]
	ds_read_b64_tr_b16 v[190:191], v143 offset:40960
	v_pk_mul_f32 v[96:97], v[64:65], v[186:187] op_sel_hi:[1,0]
	v_pk_mul_f32 v[84:85], v[84:85], v[94:95]
	v_mfma_f32_16x16x32_bf16 v[66:69], v[192:195], v[8:11], v[160:163]
	v_cvt_pk_bf16_f32 v173, v96, v97
	v_pk_mul_f32 v[96:97], v[76:77], v[78:79]
	s_waitcnt lgkmcnt(11)
	v_mfma_f32_16x16x32_bf16 v[68:71], v[196:199], v[12:15], v[66:69]
	ds_read_b64_tr_b16 v[188:189], v142 offset:40960
	ds_read_b64_tr_b16 v[192:193], v136 offset:32768
	ds_read_b64_tr_b16 v[194:195], v139 offset:32768
	ds_read_b64_tr_b16 v[198:199], v139 offset:40960
	v_pk_mul_f32 v[96:97], v[96:97], v[186:187] op_sel_hi:[1,0]
	v_pk_mul_f32 v[86:87], v[86:87], v[92:93]
	v_mfma_f32_16x16x32_bf16 v[164:167], v[200:203], v[4:7], v[164:167]
	v_mul_f32_e64 v66, v184, v186
	v_mul_f32_e64 v67, v185, v186
	v_pk_mul_f32 v[80:81], v[80:81], v[82:83]
	v_cvt_pk_bf16_f32 v172, v66, v67
	v_mfma_f32_16x16x32_bf16 v[64:67], v[204:207], v[8:11], v[164:167]
	s_and_b64 vcc, exec, s[6:7]
	s_waitcnt lgkmcnt(11)
	v_mfma_f32_16x16x32_bf16 v[64:67], v[212:215], v[12:15], v[64:67]
	ds_read_b64_tr_b16 v[196:197], v136 offset:40960
	ds_read_b64_tr_b16 v[200:201], v138 offset:32768
	ds_read_b64_tr_b16 v[202:203], v141 offset:32768
	ds_read_b64_tr_b16 v[206:207], v141 offset:40960
	v_mfma_f32_16x16x32_bf16 v[168:171], v[216:219], v[0:3], 0
	v_cvt_pk_bf16_f32 v174, v96, v97
	v_pk_mul_f32 v[96:97], v[72:73], v[186:187] op_sel_hi:[1,0]
	v_mfma_f32_16x16x32_bf16 v[76:79], v[208:211], v[4:7], v[168:171]
	v_cvt_pk_bf16_f32 v175, v96, v97
	v_mfma_f32_16x16x32_bf16 v[94:97], v[224:227], v[0:3], 0
	v_mfma_f32_16x16x32_bf16 v[72:75], v[220:223], v[8:11], v[76:79]
	v_mul_f32_e32 v162, v153, v158
	v_pk_mul_f32 v[84:85], v[84:85], v[162:163] op_sel_hi:[1,0]
	v_pk_mul_f32 v[86:87], v[86:87], v[162:163] op_sel_hi:[1,0]
	s_waitcnt lgkmcnt(10)
	v_mfma_f32_16x16x32_bf16 v[92:95], v[232:235], v[4:7], v[94:97]
	ds_read_b64_tr_b16 v[204:205], v138 offset:40960
	ds_read_b64_tr_b16 v[212:213], v137 offset:32768
	ds_read_b64_tr_b16 v[214:215], v140 offset:32768
	ds_read_b64_tr_b16 v[218:219], v140 offset:40960
	ds_read_b64_tr_b16 v[216:217], v137 offset:40960
	v_cvt_pk_bf16_f32 v84, v84, v85
	v_cvt_pk_bf16_f32 v85, v86, v87
	v_pk_mul_f32 v[86:87], v[88:89], v[90:91]
	v_mfma_f32_16x16x32_bf16 v[92:95], v[236:239], v[8:11], v[92:95]
	v_pk_mul_f32 v[86:87], v[86:87], v[162:163] op_sel_hi:[1,0]
	v_mfma_f32_16x16x32_bf16 v[76:79], v[176:179], v[12:15], v[92:95]
	v_cvt_pk_bf16_f32 v86, v86, v87
	s_nop 4
	v_pk_mul_f32 v[92:93], v[80:81], v[162:163] op_sel_hi:[1,0]
	s_waitcnt lgkmcnt(11)
	v_mfma_f32_16x16x32_bf16 v[60:63], v[180:183], v[172:175], v[60:63]
	ds_read_b64_tr_b16 v[208:209], v145 offset:32768
	ds_read_b64_tr_b16 v[210:211], v146 offset:32768
	ds_read_b64_tr_b16 v[226:227], v146 offset:40960
	ds_read_b64_tr_b16 v[224:225], v145 offset:40960
	v_cvt_pk_bf16_f32 v87, v92, v93
	s_waitcnt lgkmcnt(11)
	v_mfma_f32_16x16x32_bf16 v[52:55], v[192:195], v[172:175], v[52:55]
	ds_read_b64_tr_b16 v[220:221], v147 offset:32768
	ds_read_b64_tr_b16 v[222:223], v148 offset:32768
	ds_read_b64_tr_b16 v[234:235], v148 offset:40960
	ds_read_b64_tr_b16 v[232:233], v147 offset:40960
	v_mfma_f32_16x16x32_bf16 v[52:55], v[196:199], v[84:87], v[52:55]
	s_waitcnt lgkmcnt(11)
	v_mfma_f32_16x16x32_bf16 v[44:47], v[200:203], v[172:175], v[44:47]
	ds_read_b64_tr_b16 v[236:237], v149 offset:32768
	ds_read_b64_tr_b16 v[238:239], v150 offset:32768
	ds_read_b64_tr_b16 v[178:179], v150 offset:40960
	ds_read_b64_tr_b16 v[176:177], v149 offset:40960
	v_mfma_f32_16x16x32_bf16 v[44:47], v[204:207], v[84:87], v[44:47]
	s_waitcnt lgkmcnt(11)
	v_mfma_f32_16x16x32_bf16 v[56:59], v[212:215], v[172:175], v[56:59]
	ds_read_b64_tr_b16 v[180:181], v151 offset:32768
	ds_read_b64_tr_b16 v[182:183], v152 offset:32768
	ds_read_b64_tr_b16 v[194:195], v152 offset:40960
	ds_read_b64_tr_b16 v[192:193], v151 offset:40960
	v_mfma_f32_16x16x32_bf16 v[56:59], v[216:219], v[84:87], v[56:59]
	s_waitcnt lgkmcnt(11)
	v_mfma_f32_16x16x32_bf16 v[48:51], v[208:211], v[172:175], v[48:51]
	v_mfma_f32_16x16x32_bf16 v[48:51], v[224:227], v[84:87], v[48:51]
	s_waitcnt lgkmcnt(7)
	v_mfma_f32_16x16x32_bf16 v[40:43], v[220:223], v[172:175], v[40:43]
	v_mfma_f32_16x16x32_bf16 v[40:43], v[232:235], v[84:87], v[40:43]
	s_waitcnt lgkmcnt(3)
	v_mfma_f32_16x16x32_bf16 v[32:35], v[236:239], v[172:175], v[32:35]
	v_mfma_f32_16x16x32_bf16 v[32:35], v[176:179], v[84:87], v[32:35]
	s_waitcnt lgkmcnt(0)
	v_mfma_f32_16x16x32_bf16 v[36:39], v[180:183], v[172:175], v[36:39]
	v_mfma_f32_16x16x32_bf16 v[72:75], v[228:231], v[12:15], v[72:75]
	v_mfma_f32_16x16x32_bf16 v[60:63], v[188:191], v[84:87], v[60:63]
	v_mfma_f32_16x16x32_bf16 v[36:39], v[192:195], v[84:87], v[36:39]
	s_cbranch_vccnz .LBB0_2159
	s_waitcnt vmcnt(3)
	ds_write_b128 v98, v[16:19]
	s_waitcnt vmcnt(2)
	ds_write_b128 v99, v[20:23]
	s_waitcnt vmcnt(1)
	ds_write_b128 v100, v[24:27] offset:49152
	s_waitcnt vmcnt(0)
	ds_write_b128 v124, v[28:31] offset:49152
